# attention bias v_pk_fma_f32 (op_sel_hi 1,1,0, feeding the QK MFMA accumulators) split into scalar v_fma_f32 pairs, 150 sites
# baseline (speedup 1.0000x reference)
.Lsw1_A:
	v_add_u32_e32 v66, 64, v216
	v_cvt_f32_i32_e32 v67, v66
	s_waitcnt vmcnt(0)
	v_lshrrev_b32_e32 v83, v208, v196
	v_and_b32_e32 v66, 1, v83
	v_cmp_eq_u32_e32 vcc, 1, v66
	v_mul_f32_e64 v82, -v178, v67
	v_fma_f32 v68, 0, v178, v82
	v_cndmask_b32_e32 v66, v243, v68, vcc
	v_and_b32_e32 v68, 2, v83
	v_fma_f32 v67, -v178, v67, v178
	v_cmp_ne_u32_e32 vcc, 0, v68
	v_and_b32_e32 v70, 8, v83
	v_fma_f32 v68, v188, s60, v82
	v_fma_f32 v69, v189, s61, v82
	v_cndmask_b32_e32 v67, v243, v67, vcc
	v_and_b32_e32 v71, 4, v83
	v_cmp_ne_u32_e32 vcc, 0, v70
	v_and_b32_e32 v72, 0x200, v83
	v_and_b32_e32 v73, 0x100, v83
	v_cndmask_b32_e32 v69, v243, v69, vcc
	v_cmp_ne_u32_e32 vcc, 0, v71
	v_fma_f32 v70, v188, s74, v82
	v_fma_f32 v71, v189, s75, v82
	v_and_b32_e32 v74, 0x800, v83
	v_cndmask_b32_e32 v68, v243, v68, vcc
	v_cmp_ne_u32_e32 vcc, 0, v72
	v_and_b32_e32 v75, 0x400, v83
	v_and_b32_e32 v76, 0x20000, v83
	v_cndmask_b32_e32 v71, v243, v71, vcc
	v_cmp_ne_u32_e32 vcc, 0, v73
	v_fma_f32 v72, v188, s62, v82
	v_fma_f32 v73, v189, s63, v82
	v_and_b32_e32 v77, 0x10000, v83
	v_cndmask_b32_e32 v70, v243, v70, vcc
	v_cmp_ne_u32_e32 vcc, 0, v74
	s_mov_b32 s2, 0x41900000
	s_mov_b32 s3, 0x41980000
	v_cndmask_b32_e32 v73, v243, v73, vcc
	v_cmp_ne_u32_e32 vcc, 0, v75
	v_fma_f32 v74, v188, s58, v82
	v_fma_f32 v75, v189, s59, v82
	v_and_b32_e32 v78, 0x80000, v83
	v_cndmask_b32_e32 v72, v243, v72, vcc
	v_cmp_ne_u32_e32 vcc, 0, v76
	v_and_b32_e32 v79, 0x40000, v83
	v_and_b32_e32 v80, 0x2000000, v83
	v_cndmask_b32_e32 v75, v243, v75, vcc
	v_cmp_ne_u32_e32 vcc, 0, v77
	v_fma_f32 v76, v188, s2, v82
	v_fma_f32 v77, v189, s3, v82
	s_mov_b32 s2, 0x41c00000
	v_cndmask_b32_e32 v74, v243, v74, vcc
	v_cmp_ne_u32_e32 vcc, 0, v78
	s_mov_b32 s3, 0x41c80000
	v_and_b32_e32 v81, 0x1000000, v83
	v_cndmask_b32_e32 v77, v243, v77, vcc
	v_cmp_ne_u32_e32 vcc, 0, v79
	v_fma_f32 v78, v188, s2, v82
	v_fma_f32 v79, v189, s3, v82
	s_mov_b32 s2, 0x41d00000
	v_cndmask_b32_e32 v76, v243, v76, vcc
	v_cmp_ne_u32_e32 vcc, 0, v80
	s_mov_b32 s3, 0x41d80000
	v_and_b32_e32 v84, 0x8000000, v83
	v_cndmask_b32_e32 v79, v243, v79, vcc
	v_cmp_ne_u32_e32 vcc, 0, v81
	v_lshrrev_b32_e32 v98, v208, v197
	v_fma_f32 v80, v188, s2, v82
	v_fma_f32 v81, v189, s3, v82
	v_cndmask_b32_e32 v78, v243, v78, vcc
	v_and_b32_e32 v83, 0x4000000, v83
	v_cmp_ne_u32_e32 vcc, 0, v84
	v_and_b32_e32 v99, 0x8000000, v98
	v_fma_f32 v96, v188, s68, v82
	v_fma_f32 v97, v189, s69, v82
	v_cndmask_b32_e32 v81, v243, v81, vcc
	v_cmp_ne_u32_e32 vcc, 0, v83
	v_fma_f32 v94, v188, s96, v82
	v_fma_f32 v95, v189, s97, v82
	v_fma_f32 v92, v188, s94, v82
	v_fma_f32 v93, v189, s95, v82
	v_cndmask_b32_e32 v80, v243, v80, vcc
	v_cmp_ne_u32_e32 vcc, 0, v99
	v_and_b32_e32 v99, 0x4000000, v98
	v_fma_f32 v90, v188, s92, v82
	v_fma_f32 v91, v189, s93, v82
	v_cndmask_b32_e32 v97, v243, v97, vcc
	v_cmp_ne_u32_e32 vcc, 0, v99
	v_and_b32_e32 v99, 0x2000000, v98
	v_fma_f32 v88, v188, s90, v82
	v_fma_f32 v89, v189, s91, v82
	v_cndmask_b32_e32 v96, v243, v96, vcc
	v_cmp_ne_u32_e32 vcc, 0, v99
	v_and_b32_e32 v99, 0x1000000, v98
	v_fma_f32 v86, v188, s88, v82
	v_fma_f32 v87, v189, s89, v82
	v_cndmask_b32_e32 v95, v243, v95, vcc
	v_cmp_ne_u32_e32 vcc, 0, v99
	v_and_b32_e32 v99, 0x80000, v98
	v_fma_f32 v84, v188, s86, v82
	v_fma_f32 v85, v189, s87, v82
	v_cndmask_b32_e32 v94, v243, v94, vcc
	v_cmp_ne_u32_e32 vcc, 0, v99
	v_and_b32_e32 v99, 0x40000, v98
	s_mov_b32 s2, 0x42000000
	v_cndmask_b32_e32 v93, v243, v93, vcc
	v_cmp_ne_u32_e32 vcc, 0, v99
	v_and_b32_e32 v99, 0x20000, v98
	s_mov_b32 s3, 0x42040000
	v_cndmask_b32_e32 v92, v243, v92, vcc
	v_cmp_ne_u32_e32 vcc, 0, v99
	v_and_b32_e32 v99, 0x10000, v98
	v_fma_f32 v83, v185, s3, v82
	v_fma_f32 v82, v184, s2, v82
	v_cndmask_b32_e32 v91, v243, v91, vcc
	v_cmp_ne_u32_e32 vcc, 0, v99
	v_and_b32_e32 v99, 0x800, v98
	s_nop 0
	v_cndmask_b32_e32 v90, v243, v90, vcc
	v_cmp_ne_u32_e32 vcc, 0, v99
	v_and_b32_e32 v99, 0x400, v98
	s_nop 0
	v_cndmask_b32_e32 v89, v243, v89, vcc
	v_cmp_ne_u32_e32 vcc, 0, v99
	v_and_b32_e32 v99, 0x200, v98
	s_nop 0
	v_cndmask_b32_e32 v88, v243, v88, vcc
	v_cmp_ne_u32_e32 vcc, 0, v99
	v_and_b32_e32 v99, 0x100, v98
	s_nop 0
	v_cndmask_b32_e32 v87, v243, v87, vcc
	v_cmp_ne_u32_e32 vcc, 0, v99
	v_and_b32_e32 v99, 8, v98
	s_nop 0
	v_cndmask_b32_e32 v86, v243, v86, vcc
	v_cmp_ne_u32_e32 vcc, 0, v99
	v_and_b32_e32 v99, 4, v98
	s_nop 0
	v_cndmask_b32_e32 v85, v243, v85, vcc
	v_cmp_ne_u32_e32 vcc, 0, v99
	v_and_b32_e32 v99, 2, v98
	v_and_b32_e32 v98, 1, v98
	v_cndmask_b32_e32 v84, v243, v84, vcc
	v_cmp_ne_u32_e32 vcc, 0, v99
	s_nop 1
	v_cndmask_b32_e32 v83, v243, v83, vcc
	v_cmp_eq_u32_e32 vcc, 1, v98
	s_nop 1
	v_cndmask_b32_e32 v82, v243, v82, vcc
	s_setprio 1
	ds_read_b128 v[114:117], v211 offset:49152
	ds_read_b128 v[124:127], v211 offset:57344
	s_waitcnt lgkmcnt(1)
	v_mfma_f32_32x32x16_bf16 v[66:81], v[114:117], v[158:161], v[66:81]
	ds_read_b128 v[114:117], v212 offset:49152
	s_waitcnt lgkmcnt(1)
	v_mfma_f32_32x32x16_bf16 v[82:97], v[124:127], v[158:161], v[82:97]
	ds_read_b128 v[124:127], v212 offset:57344
	s_waitcnt lgkmcnt(1)
	v_mfma_f32_32x32x16_bf16 v[66:81], v[114:117], v[154:157], v[66:81]
	ds_read_b128 v[114:117], v213 offset:49152
	s_waitcnt lgkmcnt(1)
	v_mfma_f32_32x32x16_bf16 v[82:97], v[124:127], v[154:157], v[82:97]
	ds_read_b128 v[124:127], v213 offset:57344
	s_waitcnt lgkmcnt(1)
	v_mfma_f32_32x32x16_bf16 v[66:81], v[114:117], v[150:153], v[66:81]
	ds_read_b128 v[114:117], v214 offset:49152
	s_waitcnt lgkmcnt(1)
	v_mfma_f32_32x32x16_bf16 v[82:97], v[124:127], v[150:153], v[82:97]
	ds_read_b128 v[124:127], v214 offset:57344
	s_waitcnt lgkmcnt(1)
	v_mfma_f32_32x32x16_bf16 v[66:81], v[114:117], v[146:149], v[66:81]
	ds_read_b128 v[114:117], v211 offset:49280
	s_waitcnt lgkmcnt(1)
	v_mfma_f32_32x32x16_bf16 v[82:97], v[124:127], v[146:149], v[82:97]
	ds_read_b128 v[124:127], v211 offset:57472
	s_waitcnt lgkmcnt(1)
	v_mfma_f32_32x32x16_bf16 v[66:81], v[114:117], v[142:145], v[66:81]
	ds_read_b128 v[114:117], v212 offset:49280
	s_waitcnt lgkmcnt(1)
	v_mfma_f32_32x32x16_bf16 v[82:97], v[124:127], v[142:145], v[82:97]
	ds_read_b128 v[124:127], v212 offset:57472
	s_waitcnt lgkmcnt(1)
	v_mfma_f32_32x32x16_bf16 v[66:81], v[114:117], v[138:141], v[66:81]
	ds_read_b128 v[114:117], v213 offset:49280
	s_waitcnt lgkmcnt(1)
	v_mfma_f32_32x32x16_bf16 v[82:97], v[124:127], v[138:141], v[82:97]
	ds_read_b128 v[124:127], v213 offset:57472
	s_waitcnt lgkmcnt(1)
	v_mfma_f32_32x32x16_bf16 v[66:81], v[114:117], v[134:137], v[66:81]
	ds_read_b128 v[114:117], v214 offset:49280
	s_waitcnt lgkmcnt(1)
	v_mfma_f32_32x32x16_bf16 v[82:97], v[124:127], v[134:137], v[82:97]
	ds_read_b128 v[124:127], v214 offset:57472
	s_waitcnt lgkmcnt(1)
	v_mfma_f32_32x32x16_bf16 v[66:81], v[114:117], v[130:133], v[66:81]
	s_waitcnt lgkmcnt(0)
	v_mfma_f32_32x32x16_bf16 v[82:97], v[124:127], v[130:133], v[82:97]
	s_setprio 0
	global_load_dwordx2 v[196:197], v[194:195], off
	v_readlane_b32 vcc_lo, v255, 63
	s_bitcmp1_b32 vcc_lo, 0
	s_cbranch_scc1 .Lsw1_done

.LBB0_1147:
	s_waitcnt lgkmcnt(0)
	s_barrier
	v_cvt_f32_i32_e32 v99, v216
	v_lshrrev_b32_e32 v115, v208, v196
	v_and_b32_e32 v98, 1, v115
	v_cmp_eq_u32_e32 vcc, 1, v98
	v_mul_f32_e64 v114, -v178, v99
	v_fma_f32 v100, 0, v178, v114
	v_cndmask_b32_e32 v98, v243, v100, vcc
	v_and_b32_e32 v100, 2, v115
	v_fma_f32 v99, -v178, v99, v178
	v_cmp_ne_u32_e32 vcc, 0, v100
	v_and_b32_e32 v102, 8, v115
	v_fma_f32 v100, v188, s60, v114
	v_fma_f32 v101, v189, s61, v114
	v_cndmask_b32_e32 v99, v243, v99, vcc
	v_and_b32_e32 v103, 4, v115
	v_cmp_ne_u32_e32 vcc, 0, v102
	v_and_b32_e32 v104, 0x200, v115
	v_and_b32_e32 v105, 0x100, v115
	v_cndmask_b32_e32 v101, v243, v101, vcc
	v_cmp_ne_u32_e32 vcc, 0, v103
	v_fma_f32 v102, v188, s74, v114
	v_fma_f32 v103, v189, s75, v114
	v_and_b32_e32 v106, 0x800, v115
	v_cndmask_b32_e32 v100, v243, v100, vcc
	v_cmp_ne_u32_e32 vcc, 0, v104
	v_and_b32_e32 v107, 0x400, v115
	v_and_b32_e32 v108, 0x20000, v115
	v_cndmask_b32_e32 v103, v243, v103, vcc
	v_cmp_ne_u32_e32 vcc, 0, v105
	v_fma_f32 v104, v188, s62, v114
	v_fma_f32 v105, v189, s63, v114
	v_and_b32_e32 v109, 0x10000, v115
	v_cndmask_b32_e32 v102, v243, v102, vcc
	v_cmp_ne_u32_e32 vcc, 0, v106
	s_mov_b32 s4, 0x41900000
	s_mov_b32 s5, 0x41980000
	v_cndmask_b32_e32 v105, v243, v105, vcc
	v_cmp_ne_u32_e32 vcc, 0, v107
	v_fma_f32 v106, v188, s58, v114
	v_fma_f32 v107, v189, s59, v114
	v_and_b32_e32 v110, 0x80000, v115
	v_cndmask_b32_e32 v104, v243, v104, vcc
	v_cmp_ne_u32_e32 vcc, 0, v108
	v_and_b32_e32 v111, 0x40000, v115
	v_and_b32_e32 v112, 0x2000000, v115
	v_cndmask_b32_e32 v107, v243, v107, vcc
	v_cmp_ne_u32_e32 vcc, 0, v109
	v_fma_f32 v108, v188, s4, v114
	v_fma_f32 v109, v189, s5, v114
	s_mov_b32 s4, 0x41c00000
	v_cndmask_b32_e32 v106, v243, v106, vcc
	v_cmp_ne_u32_e32 vcc, 0, v110
	s_mov_b32 s5, 0x41c80000
	v_and_b32_e32 v113, 0x1000000, v115
	v_cndmask_b32_e32 v109, v243, v109, vcc
	v_cmp_ne_u32_e32 vcc, 0, v111
	v_fma_f32 v110, v188, s4, v114
	v_fma_f32 v111, v189, s5, v114
	s_mov_b32 s4, 0x41d00000
	v_cndmask_b32_e32 v108, v243, v108, vcc
	v_cmp_ne_u32_e32 vcc, 0, v112
	s_mov_b32 s5, 0x41d80000
	v_and_b32_e32 v116, 0x8000000, v115
	v_cndmask_b32_e32 v111, v243, v111, vcc
	v_cmp_ne_u32_e32 vcc, 0, v113
	v_lshrrev_b32_e32 v223, v208, v197
	v_fma_f32 v112, v188, s4, v114
	v_fma_f32 v113, v189, s5, v114
	v_cndmask_b32_e32 v110, v243, v110, vcc
	v_and_b32_e32 v115, 0x4000000, v115
	v_cmp_ne_u32_e32 vcc, 0, v116
	v_mov_b32_e32 v179, v178
	v_fma_f32 v116, v178, s86, v114
	v_fma_f32 v117, v179, s87, v114
	v_cndmask_b32_e32 v113, v243, v113, vcc
	v_cmp_ne_u32_e32 vcc, 0, v115
	v_fma_f32 v118, v178, s88, v114
	v_fma_f32 v119, v179, s89, v114
	v_fma_f32 v120, v178, s90, v114
	v_fma_f32 v121, v179, s91, v114
	v_fma_f32 v122, v178, s92, v114
	v_fma_f32 v123, v179, s93, v114
	v_fma_f32 v124, v178, s94, v114
	v_fma_f32 v125, v179, s95, v114
	v_fma_f32 v126, v178, s96, v114
	v_fma_f32 v127, v179, s97, v114
	v_fma_f32 v128, v178, s68, v114
	v_fma_f32 v129, v179, s69, v114
	v_and_b32_e32 v179, 0x8000000, v223
	v_cndmask_b32_e32 v112, v243, v112, vcc
	v_cmp_ne_u32_e32 vcc, 0, v179
	v_and_b32_e32 v179, 0x4000000, v223
	s_mov_b32 s4, 0x42000000
	v_cndmask_b32_e32 v129, v243, v129, vcc
	v_cmp_ne_u32_e32 vcc, 0, v179
	v_and_b32_e32 v179, 0x2000000, v223
	s_mov_b32 s5, 0x42040000
	v_cndmask_b32_e32 v128, v243, v128, vcc
	v_cmp_ne_u32_e32 vcc, 0, v179
	v_and_b32_e32 v179, 0x1000000, v223
	v_fma_f32 v115, v185, s5, v114
	v_fma_f32 v114, v184, s4, v114
	v_cndmask_b32_e32 v127, v243, v127, vcc
	v_cmp_ne_u32_e32 vcc, 0, v179
	v_and_b32_e32 v179, 0x80000, v223
	s_nop 0
	v_cndmask_b32_e32 v126, v243, v126, vcc
	v_cmp_ne_u32_e32 vcc, 0, v179
	v_and_b32_e32 v179, 0x40000, v223
	s_nop 0
	v_cndmask_b32_e32 v125, v243, v125, vcc
	v_cmp_ne_u32_e32 vcc, 0, v179
	v_and_b32_e32 v179, 0x20000, v223
	s_nop 0
	v_cndmask_b32_e32 v124, v243, v124, vcc
	v_cmp_ne_u32_e32 vcc, 0, v179
	v_and_b32_e32 v179, 0x10000, v223
	s_nop 0
	v_cndmask_b32_e32 v123, v243, v123, vcc
	v_cmp_ne_u32_e32 vcc, 0, v179
	v_and_b32_e32 v179, 0x800, v223
	s_nop 0
	v_cndmask_b32_e32 v122, v243, v122, vcc
	v_cmp_ne_u32_e32 vcc, 0, v179
	v_and_b32_e32 v179, 0x400, v223
	s_nop 0
	v_cndmask_b32_e32 v121, v243, v121, vcc
	v_cmp_ne_u32_e32 vcc, 0, v179
	v_and_b32_e32 v179, 0x200, v223
	s_nop 0
	v_cndmask_b32_e32 v120, v243, v120, vcc
	v_cmp_ne_u32_e32 vcc, 0, v179
	v_and_b32_e32 v179, 0x100, v223
	s_nop 0
	v_cndmask_b32_e32 v119, v243, v119, vcc
	v_cmp_ne_u32_e32 vcc, 0, v179
	v_and_b32_e32 v179, 8, v223
	s_nop 0
	v_cndmask_b32_e32 v118, v243, v118, vcc
	v_cmp_ne_u32_e32 vcc, 0, v179
	v_and_b32_e32 v179, 4, v223
	s_nop 0
	v_cndmask_b32_e32 v117, v243, v117, vcc
	v_cmp_ne_u32_e32 vcc, 0, v179
	v_and_b32_e32 v179, 2, v223
	s_nop 0
	v_cndmask_b32_e32 v116, v243, v116, vcc
	v_cmp_ne_u32_e32 vcc, 0, v179
	v_and_b32_e32 v179, 1, v223
	s_nop 0
	v_cndmask_b32_e32 v115, v243, v115, vcc
	v_cmp_eq_u32_e32 vcc, 1, v179
	s_nop 1
	v_cndmask_b32_e32 v114, v243, v114, vcc
	s_setprio 1
	ds_read_b128 v[224:227], v211 offset:32768
	ds_read_b128 v[228:231], v211 offset:40960
	s_waitcnt lgkmcnt(1)
	v_mfma_f32_32x32x16_bf16 v[98:113], v[224:227], v[158:161], v[98:113]
	ds_read_b128 v[224:227], v212 offset:32768
	s_waitcnt lgkmcnt(1)
	v_mfma_f32_32x32x16_bf16 v[114:129], v[228:231], v[158:161], v[114:129]
	ds_read_b128 v[228:231], v212 offset:40960
	s_waitcnt lgkmcnt(1)
	v_mfma_f32_32x32x16_bf16 v[98:113], v[224:227], v[154:157], v[98:113]
	ds_read_b128 v[224:227], v213 offset:32768
	s_waitcnt lgkmcnt(1)
	v_mfma_f32_32x32x16_bf16 v[114:129], v[228:231], v[154:157], v[114:129]
	ds_read_b128 v[228:231], v213 offset:40960
	s_waitcnt lgkmcnt(1)
	v_mfma_f32_32x32x16_bf16 v[98:113], v[224:227], v[150:153], v[98:113]
	ds_read_b128 v[224:227], v214 offset:32768
	s_waitcnt lgkmcnt(1)
	v_mfma_f32_32x32x16_bf16 v[114:129], v[228:231], v[150:153], v[114:129]
	ds_read_b128 v[228:231], v214 offset:40960
	s_waitcnt lgkmcnt(1)
	v_mfma_f32_32x32x16_bf16 v[98:113], v[224:227], v[146:149], v[98:113]
	ds_read_b128 v[224:227], v211 offset:32896
	s_waitcnt lgkmcnt(1)
	v_mfma_f32_32x32x16_bf16 v[114:129], v[228:231], v[146:149], v[114:129]
	ds_read_b128 v[228:231], v211 offset:41088
	s_waitcnt lgkmcnt(1)
	v_mfma_f32_32x32x16_bf16 v[98:113], v[224:227], v[142:145], v[98:113]
	ds_read_b128 v[224:227], v212 offset:32896
	s_waitcnt lgkmcnt(1)
	v_mfma_f32_32x32x16_bf16 v[114:129], v[228:231], v[142:145], v[114:129]
	ds_read_b128 v[228:231], v212 offset:41088
	s_waitcnt lgkmcnt(1)
	v_mfma_f32_32x32x16_bf16 v[98:113], v[224:227], v[138:141], v[98:113]
	ds_read_b128 v[224:227], v213 offset:32896
	s_waitcnt lgkmcnt(1)
	v_mfma_f32_32x32x16_bf16 v[114:129], v[228:231], v[138:141], v[114:129]
	ds_read_b128 v[228:231], v213 offset:41088
	s_waitcnt lgkmcnt(1)
	v_mfma_f32_32x32x16_bf16 v[98:113], v[224:227], v[134:137], v[98:113]
	ds_read_b128 v[224:227], v214 offset:32896
	s_waitcnt lgkmcnt(1)
	v_mfma_f32_32x32x16_bf16 v[114:129], v[228:231], v[134:137], v[114:129]
	ds_read_b128 v[228:231], v214 offset:41088
	s_waitcnt lgkmcnt(1)
	v_mfma_f32_32x32x16_bf16 v[98:113], v[224:227], v[130:133], v[98:113]
	s_waitcnt lgkmcnt(0)
	v_mfma_f32_32x32x16_bf16 v[114:129], v[228:231], v[130:133], v[114:129]
	s_setprio 0
	s_add_i32 s55, s53, 1
	s_cmp_lt_u32 s55, s54
	s_cselect_b64 s[4:5], -1, 0
	s_cmp_ge_u32 s55, s54
	s_cbranch_scc1 .LBB0_1149
	global_load_dwordx2 v[196:197], v[194:195], off offset:8

.LBB0_1159:
	v_add_u32_e32 v110, 32, v187
	s_andn2_b32 s52, s52, 63
	v_subrev_u32_e32 v66, s52, v209
	v_add_u32_e32 v66, 64, v66
	v_cvt_f32_i32_e32 v67, v66
	v_lshrrev_b32_e32 v82, v208, v196
	v_and_b32_e32 v66, 1, v82
	v_cmp_eq_u32_e32 vcc, 1, v66
	v_mul_f32_e64 v128, -v178, v67
	v_fma_f32 v68, 0, v178, v128
	v_cndmask_b32_e32 v66, v243, v68, vcc
	v_and_b32_e32 v68, 2, v82
	v_fma_f32 v67, -v178, v67, v178
	v_cmp_ne_u32_e32 vcc, 0, v68
	v_and_b32_e32 v70, 8, v82
	v_fma_f32 v68, v188, s60, v128
	v_fma_f32 v69, v189, s61, v128
	v_cndmask_b32_e32 v67, v243, v67, vcc
	v_and_b32_e32 v71, 4, v82
	v_cmp_ne_u32_e32 vcc, 0, v70
	v_and_b32_e32 v72, 0x200, v82
	v_and_b32_e32 v73, 0x100, v82
	v_cndmask_b32_e32 v69, v243, v69, vcc
	v_cmp_ne_u32_e32 vcc, 0, v71
	v_fma_f32 v70, v188, s74, v128
	v_fma_f32 v71, v189, s75, v128
	v_and_b32_e32 v74, 0x800, v82
	v_cndmask_b32_e32 v68, v243, v68, vcc
	v_cmp_ne_u32_e32 vcc, 0, v72
	v_and_b32_e32 v75, 0x400, v82
	v_and_b32_e32 v76, 0x20000, v82
	v_cndmask_b32_e32 v71, v243, v71, vcc
	v_cmp_ne_u32_e32 vcc, 0, v73
	v_fma_f32 v72, v188, s62, v128
	v_fma_f32 v73, v189, s63, v128
	v_and_b32_e32 v77, 0x10000, v82
	v_cndmask_b32_e32 v70, v243, v70, vcc
	v_cmp_ne_u32_e32 vcc, 0, v74
	s_mov_b32 s2, 0x41900000
	s_mov_b32 s3, 0x41980000
	v_cndmask_b32_e32 v73, v243, v73, vcc
	v_cmp_ne_u32_e32 vcc, 0, v75
	v_fma_f32 v74, v188, s58, v128
	v_fma_f32 v75, v189, s59, v128
	v_and_b32_e32 v78, 0x80000, v82
	v_cndmask_b32_e32 v72, v243, v72, vcc
	v_cmp_ne_u32_e32 vcc, 0, v76
	v_and_b32_e32 v79, 0x40000, v82
	v_and_b32_e32 v80, 0x2000000, v82
	v_cndmask_b32_e32 v75, v243, v75, vcc
	v_cmp_ne_u32_e32 vcc, 0, v77
	v_fma_f32 v76, v188, s2, v128
	v_fma_f32 v77, v189, s3, v128
	s_mov_b32 s2, 0x41c00000
	v_cndmask_b32_e32 v74, v243, v74, vcc
	v_cmp_ne_u32_e32 vcc, 0, v78
	s_mov_b32 s3, 0x41c80000
	v_and_b32_e32 v81, 0x1000000, v82
	v_cndmask_b32_e32 v77, v243, v77, vcc
	v_cmp_ne_u32_e32 vcc, 0, v79
	v_fma_f32 v78, v188, s2, v128
	v_fma_f32 v79, v189, s3, v128
	s_mov_b32 s2, 0x41d00000
	v_cndmask_b32_e32 v76, v243, v76, vcc
	v_cmp_ne_u32_e32 vcc, 0, v80
	s_mov_b32 s3, 0x41d80000
	v_and_b32_e32 v83, 0x8000000, v82
	v_cndmask_b32_e32 v79, v243, v79, vcc
	v_cmp_ne_u32_e32 vcc, 0, v81
	v_fma_f32 v80, v188, s2, v128
	v_fma_f32 v81, v189, s3, v128
	v_and_b32_e32 v82, 0x4000000, v82
	v_cndmask_b32_e32 v78, v243, v78, vcc
	v_cmp_ne_u32_e32 vcc, 0, v83
	v_lshrrev_b32_e32 v196, v208, v197
	s_nop 0
	v_cndmask_b32_e32 v81, v243, v81, vcc
	v_cmp_ne_u32_e32 vcc, 0, v82
	s_nop 1
	v_cndmask_b32_e32 v80, v243, v80, vcc
	s_setprio 1
	ds_read_b128 v[82:85], v211 offset:49152
	ds_read_b128 v[86:89], v211 offset:49280
	s_waitcnt lgkmcnt(1)
	v_mfma_f32_32x32x16_bf16 v[66:81], v[82:85], v[158:161], v[66:81]
	ds_read_b128 v[82:85], v212 offset:49152
	ds_read_b128 v[90:93], v212 offset:49280
	s_waitcnt lgkmcnt(1)
	v_mfma_f32_32x32x16_bf16 v[66:81], v[82:85], v[154:157], v[66:81]
	ds_read_b128 v[82:85], v213 offset:49152
	ds_read_b128 v[94:97], v213 offset:49280
	s_waitcnt lgkmcnt(1)
	v_mfma_f32_32x32x16_bf16 v[66:81], v[82:85], v[150:153], v[66:81]
	ds_read_b128 v[82:85], v214 offset:49152
	ds_read_b128 v[98:101], v214 offset:49280
	ds_read_b128 v[106:109], v211 offset:57344
	ds_read_b128 v[124:127], v211 offset:57472
	ds_read_b128 v[188:191], v212 offset:57344
	ds_read_b128 v[192:195], v212 offset:57472
	ds_read_b128 v[208:211], v213 offset:57344
	ds_read_b128 v[216:219], v213 offset:57472
	ds_read_b128 v[238:241], v214 offset:57344
	ds_read_b128 v[244:247], v214 offset:57472
	s_waitcnt lgkmcnt(9)
	v_mfma_f32_32x32x16_bf16 v[66:81], v[82:85], v[146:149], v[66:81]
	v_mfma_f32_32x32x16_bf16 v[66:81], v[86:89], v[142:145], v[66:81]
	v_mfma_f32_32x32x16_bf16 v[66:81], v[90:93], v[138:141], v[66:81]
	v_mfma_f32_32x32x16_bf16 v[66:81], v[94:97], v[134:137], v[66:81]
	s_waitcnt lgkmcnt(8)
	v_mfma_f32_32x32x16_bf16 v[66:81], v[98:101], v[130:133], v[66:81]
	s_setprio 0
	v_mov_b64_e32 v[82:83], s[24:25]
	v_mad_i64_i32 v[84:85], s[2:3], v187, s84, v[82:83]
	v_lshlrev_b32_e32 v86, 1, v182
	v_mov_b32_e32 v87, v1
	v_mad_i64_i32 v[82:83], s[2:3], v110, s84, v[82:83]
	v_lshl_add_u64 v[84:85], v[84:85], 0, v[86:87]
	v_lshl_add_u64 v[82:83], v[82:83], 0, v[86:87]
	global_load_dwordx4 v[98:101], v[84:85], off
	global_load_dwordx4 v[102:105], v[82:83], off
	v_mov_b64_e32 v[82:83], s[26:27]
	v_mad_i64_i32 v[84:85], s[2:3], v187, s84, v[82:83]
	v_lshl_add_u64 v[84:85], v[84:85], 0, v[86:87]
	v_mad_i64_i32 v[82:83], s[2:3], v110, s84, v[82:83]
	v_lshl_add_u64 v[82:83], v[82:83], 0, v[86:87]
	global_load_dwordx4 v[110:113], v[84:85], off
	global_load_dwordx4 v[114:117], v[82:83], off
	v_mov_b32_e32 v179, v178
	v_and_b32_e32 v96, 0x8000000, v196
	v_fma_f32 v94, v178, s68, v128
	v_fma_f32 v95, v179, s69, v128
	v_cmp_ne_u32_e32 vcc, 0, v96
	v_fma_f32 v92, v178, s96, v128
	v_fma_f32 v93, v179, s97, v128
	v_fma_f32 v90, v178, s94, v128
	v_fma_f32 v91, v179, s95, v128
	v_cndmask_b32_e32 v97, v243, v95, vcc
	v_and_b32_e32 v95, 0x4000000, v196
	v_cmp_ne_u32_e32 vcc, 0, v95
	v_fma_f32 v88, v178, s92, v128
	v_fma_f32 v89, v179, s93, v128
	v_fma_f32 v86, v178, s90, v128
	v_fma_f32 v87, v179, s91, v128
	v_cndmask_b32_e32 v96, v243, v94, vcc
	v_and_b32_e32 v94, 0x2000000, v196
	v_cmp_ne_u32_e32 vcc, 0, v94
	v_fma_f32 v84, v178, s88, v128
	v_fma_f32 v85, v179, s89, v128
	v_fma_f32 v82, v178, s86, v128
	v_fma_f32 v83, v179, s87, v128
	v_cndmask_b32_e32 v95, v243, v93, vcc
	v_and_b32_e32 v93, 0x1000000, v196
	v_cmp_ne_u32_e32 vcc, 0, v93
	s_mov_b32 s2, 0x42000000
	s_mov_b32 s3, 0x42040000
	v_cndmask_b32_e32 v94, v243, v92, vcc
	v_and_b32_e32 v92, 0x80000, v196
	v_cmp_ne_u32_e32 vcc, 0, v92
	v_fma_f32 v129, v185, s3, v128
	v_fma_f32 v128, v184, s2, v128
	v_mov_b32_e32 v187, v1
	v_cndmask_b32_e32 v93, v243, v91, vcc
	v_and_b32_e32 v91, 0x40000, v196
	v_cmp_ne_u32_e32 vcc, 0, v91
	s_nop 1
	v_cndmask_b32_e32 v92, v243, v90, vcc
	v_and_b32_e32 v90, 0x20000, v196
	v_cmp_ne_u32_e32 vcc, 0, v90
	s_nop 1
	v_cndmask_b32_e32 v91, v243, v89, vcc
	v_and_b32_e32 v89, 0x10000, v196
	v_cmp_ne_u32_e32 vcc, 0, v89
	s_nop 1
	v_cndmask_b32_e32 v90, v243, v88, vcc
	v_and_b32_e32 v88, 0x800, v196
	v_cmp_ne_u32_e32 vcc, 0, v88
	s_nop 1
	v_cndmask_b32_e32 v89, v243, v87, vcc
	v_and_b32_e32 v87, 0x400, v196
	v_cmp_ne_u32_e32 vcc, 0, v87
	s_nop 1
	v_cndmask_b32_e32 v88, v243, v86, vcc
	v_and_b32_e32 v86, 0x200, v196
	v_cmp_ne_u32_e32 vcc, 0, v86
	s_nop 1
	v_cndmask_b32_e32 v87, v243, v85, vcc
	v_and_b32_e32 v85, 0x100, v196
	v_cmp_ne_u32_e32 vcc, 0, v85
	s_nop 1
	v_cndmask_b32_e32 v86, v243, v84, vcc
	v_and_b32_e32 v84, 8, v196
	v_cmp_ne_u32_e32 vcc, 0, v84
	s_nop 1
	v_cndmask_b32_e32 v85, v243, v83, vcc
	v_and_b32_e32 v83, 4, v196
	v_cmp_ne_u32_e32 vcc, 0, v83
	s_nop 1
	v_cndmask_b32_e32 v84, v243, v82, vcc
	v_and_b32_e32 v82, 2, v196
	v_cmp_ne_u32_e32 vcc, 0, v82
	v_and_b32_e32 v82, 1, v196
	s_nop 0
	v_cndmask_b32_e32 v83, v243, v129, vcc
	v_cmp_eq_u32_e32 vcc, 1, v82
	s_nop 1
	v_cndmask_b32_e32 v82, v243, v128, vcc
	s_waitcnt lgkmcnt(7)
	s_nop 0
	v_mfma_f32_32x32x16_bf16 v[82:97], v[106:109], v[158:161], v[82:97]
	v_mov_b64_e32 v[106:107], s[20:21]
	v_mad_i64_i32 v[106:107], s[2:3], v180, s84, v[106:107]
	v_lshl_add_u64 v[106:107], v[106:107], 0, v[186:187]
	s_waitcnt lgkmcnt(5)
	v_mfma_f32_32x32x16_bf16 v[82:97], v[188:191], v[154:157], v[82:97]
	s_waitcnt lgkmcnt(3)
	v_mfma_f32_32x32x16_bf16 v[82:97], v[208:211], v[150:153], v[82:97]
	s_waitcnt lgkmcnt(1)
	v_mfma_f32_32x32x16_bf16 v[82:97], v[238:241], v[146:149], v[82:97]
	v_mfma_f32_32x32x16_bf16 v[82:97], v[124:127], v[142:145], v[82:97]
	v_mfma_f32_32x32x16_bf16 v[82:97], v[192:195], v[138:141], v[82:97]
	global_load_dwordx4 v[158:161], v[106:107], off
	global_load_dwordx4 v[154:157], v[106:107], off offset:32
	global_load_dwordx4 v[150:153], v[106:107], off offset:64
	global_load_dwordx4 v[146:149], v[106:107], off offset:96
	global_load_dwordx4 v[142:145], v[106:107], off offset:128
	global_load_dwordx4 v[138:141], v[106:107], off offset:160
	v_mfma_f32_32x32x16_bf16 v[82:97], v[216:219], v[134:137], v[82:97]
	global_load_dwordx4 v[134:137], v[106:107], off offset:192
	s_nop 0
	global_load_dwordx4 v[106:109], v[106:107], off offset:224
	s_waitcnt lgkmcnt(0)
	v_mfma_f32_32x32x16_bf16 v[82:97], v[244:247], v[130:133], v[82:97]
	v_exp_f32_e32 v128, v170
	v_exp_f32_e32 v170, v118
	v_add_f32_e32 v118, 0, v225
	v_add_f32_e32 v118, v229, v118
	v_add_f32_e32 v118, v226, v118
	v_add_f32_e32 v118, v230, v118
	v_add_f32_e32 v118, v227, v118
	v_add_f32_e32 v118, v231, v118
	v_add_f32_e32 v118, v228, v118
	v_add_f32_e32 v118, v232, v118
	v_add_f32_e32 v118, v173, v118
	v_add_f32_e32 v118, v177, v118
	v_add_f32_e32 v118, v174, v118
	v_add_f32_e32 v118, v222, v118
	v_add_f32_e32 v118, v175, v118
	v_exp_f32_e32 v129, v171
	v_add_f32_e32 v118, v223, v118
	v_exp_f32_e32 v130, v168
	v_add_f32_e32 v118, v176, v118
	v_exp_f32_e32 v131, v169
	v_add_f32_e32 v118, v224, v118
	v_exp_f32_e32 v132, v166
	v_add_f32_e32 v118, v128, v118
	v_exp_f32_e32 v133, v167
	v_add_f32_e32 v118, v129, v118
	v_exp_f32_e32 v164, v164
	v_add_f32_e32 v118, v130, v118
	v_exp_f32_e32 v165, v165
	v_add_f32_e32 v118, v131, v118
	v_exp_f32_e32 v162, v162
	v_add_f32_e32 v118, v132, v118
	v_exp_f32_e32 v163, v163
	v_add_f32_e32 v118, v133, v118
	v_exp_f32_e32 v166, v122
	v_add_f32_e32 v118, v164, v118
	v_exp_f32_e32 v167, v123
	v_add_f32_e32 v118, v165, v118
	v_exp_f32_e32 v168, v120
	v_add_f32_e32 v118, v162, v118
	v_exp_f32_e32 v169, v121
	v_add_f32_e32 v118, v163, v118
	v_add_f32_e32 v118, v166, v118
	v_exp_f32_e32 v171, v119
	v_add_f32_e32 v118, v167, v118
	v_add_f32_e32 v118, v168, v118
	v_add_f32_e32 v118, v169, v118
	v_add_f32_e32 v118, v170, v118
	v_add_f32_e32 v118, v171, v118
	v_mov_b32_e32 v119, v118
	v_cvt_pk_bf16_f32 v120, v225, v229
	v_cvt_pk_bf16_f32 v121, v226, v230
	v_cvt_pk_bf16_f32 v122, v227, v231
	v_cvt_pk_bf16_f32 v123, v228, v232
	s_nop 1
	v_permlane32_swap_b32_e32 v118, v119
	v_permlane32_swap_b32_e32 v120, v122
	v_permlane32_swap_b32_e32 v121, v123
	v_cvt_pk_bf16_f32 v124, v173, v177
	v_cvt_pk_bf16_f32 v125, v174, v222
	v_cvt_pk_bf16_f32 v126, v175, v223
	v_cvt_pk_bf16_f32 v127, v176, v224
	v_cvt_pk_bf16_f32 v128, v128, v129
	v_cvt_pk_bf16_f32 v129, v130, v131
	v_cvt_pk_bf16_f32 v130, v132, v133
	v_cvt_pk_bf16_f32 v131, v164, v165
	v_cvt_pk_bf16_f32 v162, v162, v163
	v_cvt_pk_bf16_f32 v163, v166, v167
	v_cvt_pk_bf16_f32 v164, v168, v169
	v_cvt_pk_bf16_f32 v165, v170, v171
	s_nop 0
	v_permlane32_swap_b32_e32 v124, v126
	v_permlane32_swap_b32_e32 v125, v127
	v_permlane32_swap_b32_e32 v128, v130
	v_permlane32_swap_b32_e32 v129, v131
	v_permlane32_swap_b32_e32 v162, v164
	v_permlane32_swap_b32_e32 v163, v165
	s_setprio 1
	ds_read_b64_tr_b16 v[166:167], v201 offset:0
	ds_read_b64_tr_b16 v[168:169], v201 offset:0x800
	ds_read_b64_tr_b16 v[174:175], v201 offset:0x1000
	ds_read_b64_tr_b16 v[176:177], v201 offset:0x1800
	ds_read_b64_tr_b16 v[184:185], v201 offset:0x2000
	ds_read_b64_tr_b16 v[186:187], v201 offset:0x2800
	ds_read_b64_tr_b16 v[188:189], v201 offset:0x3000
	ds_read_b64_tr_b16 v[190:191], v201 offset:0x3800
	s_waitcnt lgkmcnt(0)
	s_nop 0
	v_mfma_f32_32x32x16_bf16 v[2:17], v[120:123], v[166:169], v[2:17]
	ds_read_b64_tr_b16 v[166:167], v201 offset:0x200
	ds_read_b64_tr_b16 v[168:169], v201 offset:0xa00
	v_mfma_f32_32x32x16_bf16 v[2:17], v[124:127], v[174:177], v[2:17]
	ds_read_b64_tr_b16 v[174:175], v201 offset:0x1200
	ds_read_b64_tr_b16 v[176:177], v201 offset:0x1a00
	v_mfma_f32_32x32x16_bf16 v[2:17], v[128:131], v[184:187], v[2:17]
	ds_read_b64_tr_b16 v[184:185], v201 offset:0x2200
	ds_read_b64_tr_b16 v[186:187], v201 offset:0x2a00
	v_mfma_f32_32x32x16_bf16 v[2:17], v[162:165], v[188:191], v[2:17]
	ds_read_b64_tr_b16 v[188:189], v201 offset:0x3200
	ds_read_b64_tr_b16 v[190:191], v201 offset:0x3a00
	s_waitcnt lgkmcnt(0)
	v_mfma_f32_32x32x16_bf16 v[50:65], v[120:123], v[166:169], v[50:65]
	ds_read_b64_tr_b16 v[166:167], v201 offset:0x400
	ds_read_b64_tr_b16 v[168:169], v201 offset:0xc00
	v_mfma_f32_32x32x16_bf16 v[50:65], v[124:127], v[174:177], v[50:65]
	ds_read_b64_tr_b16 v[174:175], v201 offset:0x1400
	ds_read_b64_tr_b16 v[176:177], v201 offset:0x1c00
	v_mfma_f32_32x32x16_bf16 v[50:65], v[128:131], v[184:187], v[50:65]
	ds_read_b64_tr_b16 v[184:185], v201 offset:0x2400
	ds_read_b64_tr_b16 v[186:187], v201 offset:0x2c00
	v_mfma_f32_32x32x16_bf16 v[50:65], v[162:165], v[188:191], v[50:65]
	ds_read_b64_tr_b16 v[188:189], v201 offset:0x3400
	ds_read_b64_tr_b16 v[190:191], v201 offset:0x3c00
	s_waitcnt lgkmcnt(0)
	v_mfma_f32_32x32x16_bf16 v[34:49], v[120:123], v[166:169], v[34:49]
	ds_read_b64_tr_b16 v[166:167], v201 offset:0x600
	ds_read_b64_tr_b16 v[168:169], v201 offset:0xe00
	v_mfma_f32_32x32x16_bf16 v[34:49], v[124:127], v[174:177], v[34:49]
	ds_read_b64_tr_b16 v[174:175], v201 offset:0x1600
	ds_read_b64_tr_b16 v[176:177], v201 offset:0x1e00
	v_mfma_f32_32x32x16_bf16 v[34:49], v[128:131], v[184:187], v[34:49]
	ds_read_b64_tr_b16 v[184:185], v201 offset:0x2600
	ds_read_b64_tr_b16 v[186:187], v201 offset:0x2e00
	v_mfma_f32_32x32x16_bf16 v[34:49], v[162:165], v[188:191], v[34:49]
	ds_read_b64_tr_b16 v[188:189], v201 offset:0x3600
	ds_read_b64_tr_b16 v[190:191], v201 offset:0x3e00
	s_waitcnt lgkmcnt(0)
	v_mfma_f32_32x32x16_bf16 v[18:33], v[120:123], v[166:169], v[18:33]
	v_mfma_f32_32x32x16_bf16 v[18:33], v[124:127], v[174:177], v[18:33]
	v_mfma_f32_32x32x16_bf16 v[18:33], v[128:131], v[184:187], v[18:33]
	v_mfma_f32_32x32x16_bf16 v[18:33], v[162:165], v[188:191], v[18:33]
	s_setprio 0
	v_max_f32_e32 v120, v67, v67
	v_max_f32_e32 v121, v66, v66
	v_max_f32_e32 v120, v121, v120
	v_max3_f32 v120, v120, v68, v69
	v_max3_f32 v120, v120, v70, v71
	v_max3_f32 v120, v120, v72, v73
	v_max3_f32 v120, v120, v74, v75
	v_max3_f32 v120, v120, v76, v77
	v_max3_f32 v120, v120, v78, v79
	v_max3_f32 v120, v120, v80, v81
	v_max3_f32 v120, v120, v82, v83
	v_max3_f32 v120, v120, v84, v85
	v_max3_f32 v120, v120, v86, v87
	v_max3_f32 v120, v120, v88, v89
	v_max3_f32 v120, v120, v90, v91
	v_max3_f32 v120, v120, v92, v93
	v_max3_f32 v120, v120, v94, v95
	v_max3_f32 v120, v120, v96, v97
	v_mov_b32_e32 v121, v120
	s_nop 1
	v_permlane32_swap_b32_e32 v120, v121
	v_max_f32_e32 v121, v121, v121
	v_max_f32_e32 v120, v120, v120
	v_max_f32_e32 v120, v120, v121
	v_sub_f32_e32 v121, v120, v215
	v_mul_f32_e32 v121, 0x3db504f3, v121
	v_cmp_ge_f32_e32 vcc, s74, v121
	v_max_f32_e32 v121, v215, v215
	v_max_f32_e32 v121, v121, v120
	v_sub_f32_e32 v120, v215, v121
	v_mul_f32_e32 v120, 0x3e0293ee, v120
	v_exp_f32_e32 v120, v120
	s_cmp_eq_u64 vcc, exec
	s_cselect_b64 s[2:3], -1, 0
	s_waitcnt lgkmcnt(0)
	s_barrier
	v_cndmask_b32_e64 v120, v120, 1.0, s[2:3]
	v_cmp_gt_f32_e32 vcc, 1.0, v120
	s_cbranch_vccz .LBB0_1163
	s_and_saveexec_b64 s[4:5], s[0:1]
	ds_write_b32 v206, v120 offset:128
	s_or_b64 exec, exec, s[4:5]
	s_waitcnt lgkmcnt(0)
	ds_read_b128 v[122:125], v205 offset:224
	ds_read_b128 v[126:129], v205 offset:192
	ds_read_b128 v[130:133], v205 offset:160
	ds_read_b128 v[162:165], v205 offset:128
	s_waitcnt lgkmcnt(3)
	v_pk_mul_f32 v[16:17], v[16:17], v[124:125]
	s_waitcnt lgkmcnt(2)
	v_pk_mul_f32 v[12:13], v[12:13], v[128:129]
	s_waitcnt lgkmcnt(1)
	v_pk_mul_f32 v[8:9], v[8:9], v[132:133]
	s_waitcnt lgkmcnt(0)
	v_pk_mul_f32 v[4:5], v[4:5], v[164:165]
	v_pk_mul_f32 v[14:15], v[14:15], v[122:123]
	v_pk_mul_f32 v[10:11], v[10:11], v[126:127]
	v_pk_mul_f32 v[6:7], v[6:7], v[130:131]
	v_pk_mul_f32 v[2:3], v[2:3], v[162:163]
	v_pk_mul_f32 v[64:65], v[64:65], v[124:125]
	v_pk_mul_f32 v[60:61], v[60:61], v[128:129]
	v_pk_mul_f32 v[56:57], v[56:57], v[132:133]
	v_pk_mul_f32 v[52:53], v[52:53], v[164:165]
	v_pk_mul_f32 v[62:63], v[62:63], v[122:123]
	v_pk_mul_f32 v[58:59], v[58:59], v[126:127]
	v_pk_mul_f32 v[54:55], v[54:55], v[130:131]
	v_pk_mul_f32 v[50:51], v[50:51], v[162:163]
	v_pk_mul_f32 v[48:49], v[48:49], v[124:125]
	v_pk_mul_f32 v[44:45], v[44:45], v[128:129]
	v_pk_mul_f32 v[40:41], v[40:41], v[132:133]
	v_pk_mul_f32 v[36:37], v[36:37], v[164:165]
	v_pk_mul_f32 v[46:47], v[46:47], v[122:123]
	v_pk_mul_f32 v[42:43], v[42:43], v[126:127]
	v_pk_mul_f32 v[38:39], v[38:39], v[130:131]
	v_pk_mul_f32 v[34:35], v[34:35], v[162:163]
	v_pk_mul_f32 v[32:33], v[32:33], v[124:125]
	v_pk_mul_f32 v[28:29], v[28:29], v[128:129]
	v_pk_mul_f32 v[24:25], v[24:25], v[132:133]
	v_pk_mul_f32 v[20:21], v[20:21], v[164:165]
	v_pk_mul_f32 v[30:31], v[30:31], v[122:123]
	v_pk_mul_f32 v[26:27], v[26:27], v[126:127]
	v_pk_mul_f32 v[22:23], v[22:23], v[130:131]
	v_pk_mul_f32 v[18:19], v[18:19], v[162:163]

.Lsw0_A:
	v_add_u32_e32 v146, 64, v199
	v_cvt_f32_i32_e32 v66, v146
	s_sub_i32 s2, s85, 63
	s_lshr_b32 s2, s2, 8
	v_lshrrev_b32_sdwa v67, s2, v192 dst_sel:DWORD dst_unused:UNUSED_PAD src0_sel:DWORD src1_sel:WORD_0
	v_and_b32_e32 v67, 1, v67
	v_mul_f32_e64 v66, -v162, v66
	v_cmp_eq_u32_e32 vcc, 1, v67
	s_mov_b32 s2, 0x41900000
	s_mov_b32 s3, 0x41980000
	v_cndmask_b32_e32 v82, v243, v66, vcc
	v_fma_f32 v76, v170, s2, v82
	v_fma_f32 v77, v171, s3, v82
	s_mov_b32 s2, 0x41c00000
	s_mov_b32 s3, 0x41c80000
	v_fma_f32 v78, v170, s2, v82
	v_fma_f32 v79, v171, s3, v82
	s_mov_b32 s2, 0x41d00000
	s_mov_b32 s3, 0x41d80000
	v_fma_f32 v80, v170, s2, v82
	v_fma_f32 v81, v171, s3, v82
	s_mov_b32 s2, 0x42000000
	s_mov_b32 s3, 0x42040000
	v_fma_f32 v66, 0, v162, v82
	v_add_f32_e32 v67, v162, v82
	v_fma_f32 v68, v170, s60, v82
	v_fma_f32 v69, v171, s61, v82
	v_fma_f32 v70, v170, s74, v82
	v_fma_f32 v71, v171, s75, v82
	v_fma_f32 v72, v170, s62, v82
	v_fma_f32 v73, v171, s63, v82
	v_fma_f32 v74, v170, s58, v82
	v_fma_f32 v75, v171, s59, v82
	v_fma_f32 v96, v170, s68, v82
	v_fma_f32 v97, v171, s69, v82
	v_fma_f32 v94, v170, s96, v82
	v_fma_f32 v95, v171, s97, v82
	v_fma_f32 v92, v170, s94, v82
	v_fma_f32 v93, v171, s95, v82
	v_fma_f32 v90, v170, s92, v82
	v_fma_f32 v91, v171, s93, v82
	v_fma_f32 v88, v170, s90, v82
	v_fma_f32 v89, v171, s91, v82
	v_fma_f32 v86, v170, s88, v82
	v_fma_f32 v87, v171, s89, v82
	v_fma_f32 v84, v170, s86, v82
	v_fma_f32 v85, v171, s87, v82
	v_fma_f32 v83, v169, s3, v82
	v_fma_f32 v82, v168, s2, v82
	s_setprio 1
	ds_read_b128 v[130:133], v195 offset:49152
	ds_read_b128 v[134:137], v195 offset:57344
	ds_read_b128 v[138:141], v196 offset:49152
	ds_read_b128 v[142:145], v196 offset:57344
	s_waitcnt lgkmcnt(3)
	v_mfma_f32_32x32x16_bf16 v[66:81], v[130:133], v[126:129], v[66:81]
	ds_read_b128 v[130:133], v197 offset:49152
	s_waitcnt lgkmcnt(3)
	v_mfma_f32_32x32x16_bf16 v[82:97], v[134:137], v[126:129], v[82:97]
	ds_read_b128 v[134:137], v197 offset:57344
	s_waitcnt lgkmcnt(3)
	v_mfma_f32_32x32x16_bf16 v[66:81], v[138:141], v[122:125], v[66:81]
	ds_read_b128 v[138:141], v198 offset:49152
	s_waitcnt lgkmcnt(3)
	v_mfma_f32_32x32x16_bf16 v[82:97], v[142:145], v[122:125], v[82:97]
	ds_read_b128 v[142:145], v198 offset:57344
	s_waitcnt lgkmcnt(3)
	v_mfma_f32_32x32x16_bf16 v[66:81], v[130:133], v[118:121], v[66:81]
	ds_read_b128 v[130:133], v195 offset:49280
	s_waitcnt lgkmcnt(3)
	v_mfma_f32_32x32x16_bf16 v[82:97], v[134:137], v[118:121], v[82:97]
	ds_read_b128 v[134:137], v195 offset:57472
	s_waitcnt lgkmcnt(3)
	v_mfma_f32_32x32x16_bf16 v[66:81], v[138:141], v[114:117], v[66:81]
	ds_read_b128 v[138:141], v196 offset:49280
	s_waitcnt lgkmcnt(3)
	v_mfma_f32_32x32x16_bf16 v[82:97], v[142:145], v[114:117], v[82:97]
	ds_read_b128 v[142:145], v196 offset:57472
	s_waitcnt lgkmcnt(3)
	v_mfma_f32_32x32x16_bf16 v[66:81], v[130:133], v[110:113], v[66:81]
	ds_read_b128 v[130:133], v197 offset:49280
	s_waitcnt lgkmcnt(3)
	v_mfma_f32_32x32x16_bf16 v[82:97], v[134:137], v[110:113], v[82:97]
	ds_read_b128 v[134:137], v197 offset:57472
	s_waitcnt lgkmcnt(3)
	v_mfma_f32_32x32x16_bf16 v[66:81], v[138:141], v[106:109], v[66:81]
	ds_read_b128 v[138:141], v198 offset:49280
	s_waitcnt lgkmcnt(3)
	v_mfma_f32_32x32x16_bf16 v[82:97], v[142:145], v[106:109], v[82:97]
	ds_read_b128 v[142:145], v198 offset:57472
	s_waitcnt lgkmcnt(3)
	v_mfma_f32_32x32x16_bf16 v[66:81], v[130:133], v[102:105], v[66:81]
	s_waitcnt lgkmcnt(2)
	v_mfma_f32_32x32x16_bf16 v[82:97], v[134:137], v[102:105], v[82:97]
	s_waitcnt lgkmcnt(1)
	v_mfma_f32_32x32x16_bf16 v[66:81], v[138:141], v[98:101], v[66:81]
	s_waitcnt lgkmcnt(0)
	v_mfma_f32_32x32x16_bf16 v[82:97], v[142:145], v[98:101], v[82:97]
	s_setprio 0
	v_readlane_b32 vcc_lo, v255, 63
	s_bitcmp1_b32 vcc_lo, 0
	s_cbranch_scc1 .Lsw0_done

.LBB0_1266:
	v_cndmask_b32_e64 v176, v146, v200, s[2:3]
	s_waitcnt lgkmcnt(0)
	s_barrier
	v_mul_f32_e32 v150, 0xbe0293ee, v176
	v_fmamk_f32 v66, v66, 0x3e0293ee, v150
	v_fmamk_f32 v67, v67, 0x3e0293ee, v150
	v_fmamk_f32 v68, v68, 0x3e0293ee, v150
	v_fmamk_f32 v69, v69, 0x3e0293ee, v150
	v_fmamk_f32 v70, v70, 0x3e0293ee, v150
	v_fmamk_f32 v71, v71, 0x3e0293ee, v150
	v_fmamk_f32 v72, v72, 0x3e0293ee, v150
	v_fmamk_f32 v73, v73, 0x3e0293ee, v150
	v_fmamk_f32 v74, v74, 0x3e0293ee, v150
	v_fmamk_f32 v75, v75, 0x3e0293ee, v150
	v_fmamk_f32 v76, v76, 0x3e0293ee, v150
	v_fmamk_f32 v77, v77, 0x3e0293ee, v150
	v_fmamk_f32 v78, v78, 0x3e0293ee, v150
	v_fmamk_f32 v79, v79, 0x3e0293ee, v150
	v_fmamk_f32 v80, v80, 0x3e0293ee, v150
	v_fmamk_f32 v81, v81, 0x3e0293ee, v150
	v_fmamk_f32 v151, v82, 0x3e0293ee, v150
	v_fmamk_f32 v152, v83, 0x3e0293ee, v150
	v_fmamk_f32 v153, v84, 0x3e0293ee, v150
	v_fmamk_f32 v154, v85, 0x3e0293ee, v150
	v_fmamk_f32 v155, v86, 0x3e0293ee, v150
	v_fmamk_f32 v156, v87, 0x3e0293ee, v150
	v_fmamk_f32 v157, v88, 0x3e0293ee, v150
	v_fmamk_f32 v158, v89, 0x3e0293ee, v150
	v_fmamk_f32 v159, v90, 0x3e0293ee, v150
	v_fmamk_f32 v160, v91, 0x3e0293ee, v150
	v_fmamk_f32 v161, v92, 0x3e0293ee, v150
	v_fmamk_f32 v178, v93, 0x3e0293ee, v150
	v_fmamk_f32 v179, v94, 0x3e0293ee, v150
	v_fmamk_f32 v200, v95, 0x3e0293ee, v150
	v_fmamk_f32 v206, v96, 0x3e0293ee, v150
	v_fmac_f32_e32 v150, 0x3e0293ee, v97
	v_exp_f32_e32 v208, v66
	v_exp_f32_e32 v209, v67
	v_exp_f32_e32 v210, v68
	v_exp_f32_e32 v211, v69
	v_exp_f32_e32 v212, v70
	v_exp_f32_e32 v213, v71
	v_exp_f32_e32 v214, v72
	v_exp_f32_e32 v215, v73
	v_exp_f32_e32 v216, v74
	v_exp_f32_e32 v217, v75
	v_exp_f32_e32 v218, v76
	v_exp_f32_e32 v219, v77
	v_exp_f32_e32 v220, v78
	v_exp_f32_e32 v221, v79
	v_exp_f32_e32 v222, v80
	v_exp_f32_e32 v223, v81
	s_add_i32 s2, s85, 1
	v_cvt_f32_i32_e32 v66, v199
	s_lshr_b32 s2, s2, 8
	v_lshrrev_b32_sdwa v67, s2, v192 dst_sel:DWORD dst_unused:UNUSED_PAD src0_sel:DWORD src1_sel:WORD_0
	v_and_b32_e32 v67, 1, v67
	v_mul_f32_e64 v66, -v162, v66
	v_cmp_eq_u32_e32 vcc, 1, v67
	s_mov_b32 s2, 0x41900000
	s_mov_b32 s3, 0x41980000
	v_cndmask_b32_e32 v82, v243, v66, vcc
	v_fma_f32 v76, v170, s2, v82
	v_fma_f32 v77, v171, s3, v82
	s_mov_b32 s2, 0x41c00000
	s_mov_b32 s3, 0x41c80000
	v_fma_f32 v78, v170, s2, v82
	v_fma_f32 v79, v171, s3, v82
	s_mov_b32 s2, 0x41d00000
	s_mov_b32 s3, 0x41d80000
	v_fma_f32 v80, v170, s2, v82
	v_fma_f32 v81, v171, s3, v82
	s_mov_b32 s2, 0x42000000
	v_mov_b32_e32 v163, v162
	s_mov_b32 s3, 0x42040000
	v_fma_f32 v66, 0, v162, v82
	v_add_f32_e32 v67, v162, v82
	v_fma_f32 v68, v170, s60, v82
	v_fma_f32 v69, v171, s61, v82
	v_fma_f32 v70, v170, s74, v82
	v_fma_f32 v71, v171, s75, v82
	v_fma_f32 v72, v170, s62, v82
	v_fma_f32 v73, v171, s63, v82
	v_fma_f32 v74, v170, s58, v82
	v_fma_f32 v75, v171, s59, v82
	v_fma_f32 v96, v162, s68, v82
	v_fma_f32 v97, v163, s69, v82
	v_fma_f32 v94, v162, s96, v82
	v_fma_f32 v95, v163, s97, v82
	v_fma_f32 v92, v162, s94, v82
	v_fma_f32 v93, v163, s95, v82
	v_fma_f32 v90, v162, s92, v82
	v_fma_f32 v91, v163, s93, v82
	v_fma_f32 v88, v162, s90, v82
	v_fma_f32 v89, v163, s91, v82
	v_fma_f32 v86, v162, s88, v82
	v_fma_f32 v87, v163, s89, v82
	v_fma_f32 v84, v162, s86, v82
	v_fma_f32 v85, v163, s87, v82
	v_fma_f32 v83, v169, s3, v82
	v_fma_f32 v82, v168, s2, v82
	s_setprio 1
	ds_read_b128 v[146:149], v195 offset:32768
	ds_read_b128 v[224:227], v195 offset:40960
	s_waitcnt lgkmcnt(1)
	v_mfma_f32_32x32x16_bf16 v[66:81], v[146:149], v[126:129], v[66:81]
	ds_read_b128 v[146:149], v196 offset:32768
	s_waitcnt lgkmcnt(1)
	v_mfma_f32_32x32x16_bf16 v[82:97], v[224:227], v[126:129], v[82:97]
	ds_read_b128 v[224:227], v196 offset:40960
	s_waitcnt lgkmcnt(1)
	v_mfma_f32_32x32x16_bf16 v[66:81], v[146:149], v[122:125], v[66:81]
	ds_read_b128 v[146:149], v197 offset:32768
	s_waitcnt lgkmcnt(1)
	v_mfma_f32_32x32x16_bf16 v[82:97], v[224:227], v[122:125], v[82:97]
	ds_read_b128 v[224:227], v197 offset:40960
	s_waitcnt lgkmcnt(1)
	v_mfma_f32_32x32x16_bf16 v[66:81], v[146:149], v[118:121], v[66:81]
	ds_read_b128 v[146:149], v198 offset:32768
	s_waitcnt lgkmcnt(1)
	v_mfma_f32_32x32x16_bf16 v[82:97], v[224:227], v[118:121], v[82:97]
	ds_read_b128 v[224:227], v198 offset:40960
	s_waitcnt lgkmcnt(1)
	v_mfma_f32_32x32x16_bf16 v[66:81], v[146:149], v[114:117], v[66:81]
	ds_read_b128 v[146:149], v195 offset:32896
	s_waitcnt lgkmcnt(1)
	v_mfma_f32_32x32x16_bf16 v[82:97], v[224:227], v[114:117], v[82:97]
	ds_read_b128 v[224:227], v195 offset:41088
	s_waitcnt lgkmcnt(1)
	v_mfma_f32_32x32x16_bf16 v[66:81], v[146:149], v[110:113], v[66:81]
	ds_read_b128 v[146:149], v196 offset:32896
	s_waitcnt lgkmcnt(1)
	v_mfma_f32_32x32x16_bf16 v[82:97], v[224:227], v[110:113], v[82:97]
	ds_read_b128 v[224:227], v196 offset:41088
	s_waitcnt lgkmcnt(1)
	v_mfma_f32_32x32x16_bf16 v[66:81], v[146:149], v[106:109], v[66:81]
	ds_read_b128 v[146:149], v197 offset:32896
	s_waitcnt lgkmcnt(1)
	v_mfma_f32_32x32x16_bf16 v[82:97], v[224:227], v[106:109], v[82:97]
	ds_read_b128 v[224:227], v197 offset:41088
	s_waitcnt lgkmcnt(1)
	v_mfma_f32_32x32x16_bf16 v[66:81], v[146:149], v[102:105], v[66:81]
	ds_read_b128 v[146:149], v198 offset:32896
	s_waitcnt lgkmcnt(1)
	v_mfma_f32_32x32x16_bf16 v[82:97], v[224:227], v[102:105], v[82:97]
	ds_read_b128 v[224:227], v198 offset:41088
	s_waitcnt lgkmcnt(1)
	v_mfma_f32_32x32x16_bf16 v[66:81], v[146:149], v[98:101], v[66:81]
	s_waitcnt lgkmcnt(0)
	v_mfma_f32_32x32x16_bf16 v[82:97], v[224:227], v[98:101], v[82:97]
	s_setprio 0
	v_add_f32_e32 v146, 0, v208
	v_add_f32_e32 v146, v209, v146
	v_add_f32_e32 v146, v210, v146
	v_add_f32_e32 v146, v211, v146
	v_add_f32_e32 v146, v212, v146
	v_add_f32_e32 v146, v213, v146
	v_add_f32_e32 v146, v214, v146
	v_add_f32_e32 v146, v215, v146
	v_add_f32_e32 v146, v216, v146
	v_add_f32_e32 v146, v217, v146
	v_add_f32_e32 v146, v218, v146
	v_add_f32_e32 v146, v219, v146
	v_exp_f32_e32 v225, v151
	v_add_f32_e32 v146, v220, v146
	v_exp_f32_e32 v226, v152
	v_add_f32_e32 v146, v221, v146
	v_exp_f32_e32 v227, v153
	v_add_f32_e32 v146, v222, v146
	v_exp_f32_e32 v228, v154
	v_add_f32_e32 v146, v223, v146
	v_exp_f32_e32 v229, v155
	v_add_f32_e32 v146, v225, v146
	v_exp_f32_e32 v156, v156
	v_add_f32_e32 v146, v226, v146
	v_exp_f32_e32 v157, v157
	v_add_f32_e32 v146, v227, v146
	v_exp_f32_e32 v158, v158
	v_add_f32_e32 v146, v228, v146
	v_exp_f32_e32 v159, v159
	v_add_f32_e32 v146, v229, v146
	v_exp_f32_e32 v160, v160
	v_add_f32_e32 v146, v156, v146
	v_exp_f32_e32 v161, v161
	v_add_f32_e32 v146, v157, v146
	v_exp_f32_e32 v178, v178
	v_add_f32_e32 v146, v158, v146
	v_exp_f32_e32 v179, v179
	v_add_f32_e32 v146, v159, v146
	v_exp_f32_e32 v200, v200
	v_add_f32_e32 v146, v160, v146
	v_exp_f32_e32 v206, v206
	v_add_f32_e32 v146, v161, v146
	v_exp_f32_e32 v230, v150
	v_add_f32_e32 v146, v178, v146
	v_add_f32_e32 v146, v179, v146
	v_add_f32_e32 v146, v200, v146
	v_add_f32_e32 v146, v206, v146
	v_add_f32_e32 v163, v230, v146
	v_mov_b32_e32 v224, v163
	v_cvt_pk_bf16_f32 v146, v208, v209
	v_cvt_pk_bf16_f32 v147, v210, v211
	v_cvt_pk_bf16_f32 v148, v212, v213
	v_cvt_pk_bf16_f32 v149, v214, v215
	v_cvt_pk_bf16_f32 v150, v216, v217
	v_cvt_pk_bf16_f32 v151, v218, v219
	v_cvt_pk_bf16_f32 v152, v220, v221
	v_cvt_pk_bf16_f32 v153, v222, v223
	v_cvt_pk_bf16_f32 v154, v225, v226
	v_cvt_pk_bf16_f32 v155, v227, v228
	v_cvt_pk_bf16_f32 v156, v229, v156
	v_cvt_pk_bf16_f32 v157, v157, v158
	v_cvt_pk_bf16_f32 v158, v159, v160
	v_cvt_pk_bf16_f32 v159, v161, v178
	v_cvt_pk_bf16_f32 v160, v179, v200
	v_cvt_pk_bf16_f32 v161, v206, v230
	s_nop 1
	v_permlane32_swap_b32_e32 v163, v224
	v_permlane32_swap_b32_e32 v146, v148
	v_permlane32_swap_b32_e32 v147, v149
	v_permlane32_swap_b32_e32 v150, v152
	v_permlane32_swap_b32_e32 v151, v153
	v_permlane32_swap_b32_e32 v154, v156
	v_permlane32_swap_b32_e32 v155, v157
	v_permlane32_swap_b32_e32 v158, v160
	v_permlane32_swap_b32_e32 v159, v161
	s_add_i32 s2, s84, 1
	s_cmp_lt_u32 s2, s83
	s_cselect_b64 s[76:77], -1, 0
	s_cmp_ge_u32 s2, s83
	s_cbranch_scc1 .LBB0_1268
	v_add_u32_e32 v138, 0x41, v177
	v_add_u32_e32 v140, 0x61, v177
	v_mad_i64_i32 v[130:131], s[2:3], v138, s71, v[172:173]
	v_mad_i64_i32 v[134:135], s[2:3], v140, s71, v[172:173]
	v_mad_i64_i32 v[138:139], s[2:3], v138, s71, v[174:175]
	v_mad_i64_i32 v[142:143], s[2:3], v140, s71, v[174:175]
	global_load_dwordx4 v[130:133], v[130:131], off
	s_nop 0
	global_load_dwordx4 v[134:137], v[134:135], off
	s_nop 0
	global_load_dwordx4 v[138:141], v[138:139], off
	s_nop 0
	global_load_dwordx4 v[142:145], v[142:143], off

.LBB0_1278:
	s_waitcnt vmcnt(0)
	v_add_u32_e32 v142, 32, v167
	s_and_b32 s2, s82, 0xffffffc0
	s_sub_i32 s3, s2, 64
	v_subrev_u32_e32 v172, s3, v193
	v_cvt_f32_i32_e32 v66, v172
	s_lshr_b32 s3, s3, 8
	v_lshrrev_b32_sdwa v67, s3, v192 dst_sel:DWORD dst_unused:UNUSED_PAD src0_sel:DWORD src1_sel:WORD_0
	v_and_b32_e32 v67, 1, v67
	v_mul_f32_e64 v66, -v162, v66
	v_cmp_eq_u32_e32 vcc, 1, v67
	s_mov_b32 s4, 0x41900000
	s_mov_b32 s5, 0x41980000
	v_cndmask_b32_e32 v174, v243, v66, vcc
	v_fma_f32 v76, v170, s4, v174
	v_fma_f32 v77, v171, s5, v174
	s_mov_b32 s4, 0x41c00000
	s_mov_b32 s5, 0x41c80000
	v_fma_f32 v78, v170, s4, v174
	v_fma_f32 v79, v171, s5, v174
	s_mov_b32 s4, 0x41d00000
	s_mov_b32 s5, 0x41d80000
	v_fma_f32 v66, 0, v162, v174
	v_add_f32_e32 v67, v162, v174
	v_fma_f32 v68, v170, s60, v174
	v_fma_f32 v69, v171, s61, v174
	v_fma_f32 v70, v170, s74, v174
	v_fma_f32 v71, v171, s75, v174
	v_fma_f32 v72, v170, s62, v174
	v_fma_f32 v73, v171, s63, v174
	v_fma_f32 v74, v170, s58, v174
	v_fma_f32 v75, v171, s59, v174
	v_fma_f32 v80, v170, s4, v174
	v_fma_f32 v81, v171, s5, v174
	s_setprio 1
	ds_read_b128 v[82:85], v195 offset:49152
	ds_read_b128 v[86:89], v195 offset:49280
	s_waitcnt lgkmcnt(1)
	v_mfma_f32_32x32x16_bf16 v[66:81], v[82:85], v[126:129], v[66:81]
	ds_read_b128 v[82:85], v196 offset:49152
	ds_read_b128 v[90:93], v196 offset:49280
	s_waitcnt lgkmcnt(1)
	v_mfma_f32_32x32x16_bf16 v[66:81], v[82:85], v[122:125], v[66:81]
	ds_read_b128 v[82:85], v197 offset:49152
	ds_read_b128 v[94:97], v197 offset:49280
	s_waitcnt lgkmcnt(1)
	v_mfma_f32_32x32x16_bf16 v[66:81], v[82:85], v[118:121], v[66:81]
	ds_read_b128 v[82:85], v198 offset:49152
	ds_read_b128 v[130:133], v198 offset:49280
	ds_read_b128 v[138:141], v195 offset:57344
	ds_read_b128 v[192:195], v195 offset:57472
	ds_read_b128 v[224:227], v196 offset:57344
	ds_read_b128 v[228:231], v196 offset:57472
	ds_read_b128 v[238:241], v197 offset:57344
	ds_read_b128 v[244:247], v197 offset:57472
	ds_read_b128 v[250:253], v198 offset:57344
	ds_read_b128 v[196:199], v198 offset:57472
	s_waitcnt lgkmcnt(9)
	v_mfma_f32_32x32x16_bf16 v[66:81], v[82:85], v[114:117], v[66:81]
	v_mfma_f32_32x32x16_bf16 v[66:81], v[86:89], v[110:113], v[66:81]
	v_mfma_f32_32x32x16_bf16 v[66:81], v[90:93], v[106:109], v[66:81]
	v_mfma_f32_32x32x16_bf16 v[66:81], v[94:97], v[102:105], v[66:81]
	s_waitcnt lgkmcnt(8)
	v_mfma_f32_32x32x16_bf16 v[66:81], v[130:133], v[98:101], v[66:81]
	s_setprio 0
	v_readlane_b32 s4, v254, 39
	v_readlane_b32 s5, v254, 40
	s_nop 1
	v_mov_b64_e32 v[82:83], s[4:5]
	v_mad_i64_i32 v[84:85], s[4:5], v167, s71, v[82:83]
	v_mad_i64_i32 v[82:83], s[4:5], v142, s71, v[82:83]
	v_readlane_b32 s4, v254, 29
	v_lshl_add_u64 v[84:85], v[84:85], 0, v[0:1]
	v_lshl_add_u64 v[82:83], v[82:83], 0, v[0:1]
	v_readlane_b32 s5, v254, 30
	global_load_dwordx4 v[130:133], v[84:85], off
	global_load_dwordx4 v[134:137], v[82:83], off
	v_mov_b64_e32 v[82:83], s[4:5]
	v_mad_i64_i32 v[84:85], s[4:5], v167, s71, v[82:83]
	v_lshl_add_u64 v[84:85], v[84:85], 0, v[0:1]
	v_mad_i64_i32 v[82:83], s[4:5], v142, s71, v[82:83]
	v_lshl_add_u64 v[82:83], v[82:83], 0, v[0:1]
	global_load_dwordx4 v[142:145], v[84:85], off
	global_load_dwordx4 v[146:149], v[82:83], off
	s_mov_b32 s4, 0x42000000
	v_mov_b32_e32 v163, v162
	s_mov_b32 s5, 0x42040000
	v_fma_f32 v96, v162, s68, v174
	v_fma_f32 v97, v163, s69, v174
	v_fma_f32 v94, v162, s96, v174
	v_fma_f32 v95, v163, s97, v174
	v_fma_f32 v92, v162, s94, v174
	v_fma_f32 v93, v163, s95, v174
	v_fma_f32 v90, v162, s92, v174
	v_fma_f32 v91, v163, s93, v174
	v_fma_f32 v88, v162, s90, v174
	v_fma_f32 v89, v163, s91, v174
	v_fma_f32 v86, v162, s88, v174
	v_fma_f32 v87, v163, s89, v174
	v_fma_f32 v84, v162, s86, v174
	v_fma_f32 v85, v163, s87, v174
	v_fma_f32 v82, v168, s4, v174
	v_fma_f32 v83, v169, s5, v174
	v_readlane_b32 s4, v254, 21
	v_readlane_b32 s5, v254, 22
	s_waitcnt lgkmcnt(7)
	v_mfma_f32_32x32x16_bf16 v[82:97], v[138:141], v[126:129], v[82:97]
	v_mov_b32_e32 v167, v1
	s_waitcnt lgkmcnt(5)
	v_mfma_f32_32x32x16_bf16 v[82:97], v[224:227], v[122:125], v[82:97]
	s_waitcnt lgkmcnt(3)
	v_mfma_f32_32x32x16_bf16 v[82:97], v[238:241], v[118:121], v[82:97]
	s_waitcnt lgkmcnt(1)
	v_mfma_f32_32x32x16_bf16 v[82:97], v[250:253], v[114:117], v[82:97]
	v_mfma_f32_32x32x16_bf16 v[82:97], v[192:195], v[110:113], v[82:97]
	v_mov_b64_e32 v[110:111], s[4:5]
	v_mad_i64_i32 v[110:111], s[4:5], v164, s71, v[110:111]
	v_lshl_add_u64 v[138:139], v[110:111], 0, v[166:167]
	v_mfma_f32_32x32x16_bf16 v[82:97], v[228:231], v[106:109], v[82:97]
	global_load_dwordx4 v[126:129], v[138:139], off
	global_load_dwordx4 v[122:125], v[138:139], off offset:32
	global_load_dwordx4 v[118:121], v[138:139], off offset:64
	global_load_dwordx4 v[114:117], v[138:139], off offset:96
	global_load_dwordx4 v[110:113], v[138:139], off offset:128
	global_load_dwordx4 v[106:109], v[138:139], off offset:160
	v_mfma_f32_32x32x16_bf16 v[82:97], v[244:247], v[102:105], v[82:97]
	global_load_dwordx4 v[102:105], v[138:139], off offset:192
	s_nop 0
	global_load_dwordx4 v[138:141], v[138:139], off offset:224
	s_waitcnt lgkmcnt(0)
	v_mfma_f32_32x32x16_bf16 v[82:97], v[196:199], v[98:101], v[82:97]
	v_add_f32_e32 v0, 0, v216
	v_add_f32_e32 v0, v220, v0
	v_add_f32_e32 v0, v217, v0
	v_add_f32_e32 v0, v221, v0
	v_add_f32_e32 v0, v218, v0
	v_add_f32_e32 v0, v222, v0
	v_add_f32_e32 v0, v219, v0
	v_add_f32_e32 v0, v223, v0
	v_add_f32_e32 v0, v208, v0
	v_add_f32_e32 v0, v212, v0
	v_add_f32_e32 v0, v209, v0
	v_add_f32_e32 v0, v213, v0
	v_exp_f32_e32 v99, v178
	v_add_f32_e32 v0, v210, v0
	v_exp_f32_e32 v100, v179
	v_add_f32_e32 v0, v214, v0
	v_exp_f32_e32 v101, v176
	v_add_f32_e32 v0, v211, v0
	v_exp_f32_e32 v162, v177
	v_add_f32_e32 v0, v215, v0
	v_exp_f32_e32 v160, v160
	v_add_f32_e32 v0, v99, v0
	v_exp_f32_e32 v161, v161
	v_add_f32_e32 v0, v100, v0
	v_exp_f32_e32 v163, v158
	v_add_f32_e32 v0, v101, v0
	v_exp_f32_e32 v164, v159
	v_add_f32_e32 v0, v162, v0
	v_exp_f32_e32 v166, v156
	v_add_f32_e32 v0, v160, v0
	v_exp_f32_e32 v167, v157
	v_add_f32_e32 v0, v161, v0
	v_exp_f32_e32 v168, v154
	v_add_f32_e32 v0, v163, v0
	v_exp_f32_e32 v169, v155
	v_add_f32_e32 v0, v164, v0
	v_exp_f32_e32 v170, v152
	v_add_f32_e32 v0, v166, v0
	v_exp_f32_e32 v171, v153
	v_add_f32_e32 v0, v167, v0
	v_exp_f32_e32 v173, v150
	v_add_f32_e32 v0, v168, v0
	v_exp_f32_e32 v174, v151
	v_add_f32_e32 v0, v169, v0
	v_add_f32_e32 v0, v170, v0
	v_add_f32_e32 v0, v171, v0
	v_add_f32_e32 v0, v173, v0
	v_add_f32_e32 v0, v174, v0
	v_mov_b32_e32 v98, v0
	s_nop 1
	v_permlane32_swap_b32_e32 v0, v98
	v_cvt_pk_bf16_f32 v150, v216, v220
	v_cvt_pk_bf16_f32 v151, v217, v221
	v_cvt_pk_bf16_f32 v152, v218, v222
	v_cvt_pk_bf16_f32 v153, v219, v223
	v_cvt_pk_bf16_f32 v154, v208, v212
	v_cvt_pk_bf16_f32 v155, v209, v213
	v_cvt_pk_bf16_f32 v156, v210, v214
	v_cvt_pk_bf16_f32 v157, v211, v215
	v_cvt_pk_bf16_f32 v158, v99, v100
	v_cvt_pk_bf16_f32 v159, v101, v162
	v_cvt_pk_bf16_f32 v160, v160, v161
	v_cvt_pk_bf16_f32 v161, v163, v164
	v_cvt_pk_bf16_f32 v166, v166, v167
	v_cvt_pk_bf16_f32 v167, v168, v169
	v_cvt_pk_bf16_f32 v168, v170, v171
	v_cvt_pk_bf16_f32 v169, v173, v174
	s_nop 0
	v_permlane32_swap_b32_e32 v150, v152
	v_permlane32_swap_b32_e32 v151, v153
	v_permlane32_swap_b32_e32 v154, v156
	v_permlane32_swap_b32_e32 v155, v157
	v_permlane32_swap_b32_e32 v158, v160
	v_permlane32_swap_b32_e32 v159, v161
	v_permlane32_swap_b32_e32 v166, v168
	v_permlane32_swap_b32_e32 v167, v169
	s_setprio 1
	ds_read_b64_tr_b16 v[174:175], v188 offset:0
	ds_read_b64_tr_b16 v[176:177], v188 offset:0x800
	ds_read_b64_tr_b16 v[192:193], v188 offset:0x1000
	ds_read_b64_tr_b16 v[194:195], v188 offset:0x1800
	ds_read_b64_tr_b16 v[196:197], v188 offset:0x2000
	ds_read_b64_tr_b16 v[198:199], v188 offset:0x2800
	ds_read_b64_tr_b16 v[208:209], v188 offset:0x3000
	ds_read_b64_tr_b16 v[210:211], v188 offset:0x3800
	s_waitcnt lgkmcnt(0)
	s_nop 0
	v_mfma_f32_32x32x16_bf16 v[34:49], v[150:153], v[174:177], v[34:49]
	ds_read_b64_tr_b16 v[174:175], v188 offset:0x200
	ds_read_b64_tr_b16 v[176:177], v188 offset:0xa00
	v_mfma_f32_32x32x16_bf16 v[34:49], v[154:157], v[192:195], v[34:49]
	ds_read_b64_tr_b16 v[192:193], v188 offset:0x1200
	ds_read_b64_tr_b16 v[194:195], v188 offset:0x1a00
	v_mfma_f32_32x32x16_bf16 v[34:49], v[158:161], v[196:199], v[34:49]
	ds_read_b64_tr_b16 v[196:197], v188 offset:0x2200
	ds_read_b64_tr_b16 v[198:199], v188 offset:0x2a00
	v_mfma_f32_32x32x16_bf16 v[34:49], v[166:169], v[208:211], v[34:49]
	ds_read_b64_tr_b16 v[208:209], v188 offset:0x3200
	ds_read_b64_tr_b16 v[210:211], v188 offset:0x3a00
	s_waitcnt lgkmcnt(0)
	v_mfma_f32_32x32x16_bf16 v[50:65], v[150:153], v[174:177], v[50:65]
	ds_read_b64_tr_b16 v[174:175], v188 offset:0x400
	ds_read_b64_tr_b16 v[176:177], v188 offset:0xc00
	v_mfma_f32_32x32x16_bf16 v[50:65], v[154:157], v[192:195], v[50:65]
	ds_read_b64_tr_b16 v[192:193], v188 offset:0x1400
	ds_read_b64_tr_b16 v[194:195], v188 offset:0x1c00
	v_mfma_f32_32x32x16_bf16 v[50:65], v[158:161], v[196:199], v[50:65]
	ds_read_b64_tr_b16 v[196:197], v188 offset:0x2400
	ds_read_b64_tr_b16 v[198:199], v188 offset:0x2c00
	v_mfma_f32_32x32x16_bf16 v[50:65], v[166:169], v[208:211], v[50:65]
	ds_read_b64_tr_b16 v[208:209], v188 offset:0x3400
	ds_read_b64_tr_b16 v[210:211], v188 offset:0x3c00
	s_waitcnt lgkmcnt(0)
	v_mfma_f32_32x32x16_bf16 v[18:33], v[150:153], v[174:177], v[18:33]
	ds_read_b64_tr_b16 v[174:175], v188 offset:0x600
	ds_read_b64_tr_b16 v[176:177], v188 offset:0xe00
	v_mfma_f32_32x32x16_bf16 v[18:33], v[154:157], v[192:195], v[18:33]
	ds_read_b64_tr_b16 v[192:193], v188 offset:0x1600
	ds_read_b64_tr_b16 v[194:195], v188 offset:0x1e00
	v_mfma_f32_32x32x16_bf16 v[18:33], v[158:161], v[196:199], v[18:33]
	ds_read_b64_tr_b16 v[196:197], v188 offset:0x2600
	ds_read_b64_tr_b16 v[198:199], v188 offset:0x2e00
	v_mfma_f32_32x32x16_bf16 v[18:33], v[166:169], v[208:211], v[18:33]
	ds_read_b64_tr_b16 v[208:209], v188 offset:0x3600
	ds_read_b64_tr_b16 v[210:211], v188 offset:0x3e00
	s_waitcnt lgkmcnt(0)
	v_mfma_f32_32x32x16_bf16 v[2:17], v[150:153], v[174:177], v[2:17]
	v_mfma_f32_32x32x16_bf16 v[2:17], v[154:157], v[192:195], v[2:17]
	v_mfma_f32_32x32x16_bf16 v[2:17], v[158:161], v[196:199], v[2:17]
	v_mfma_f32_32x32x16_bf16 v[2:17], v[166:169], v[208:211], v[2:17]
	s_setprio 0
	s_add_i32 s2, s2, -1
	s_mov_b32 s64, 0x41200000
	s_mov_b32 s65, 0x41300000
	s_cmp_gt_i32 s2, s78
	s_cbranch_scc0 .LBB0_1280
	v_cmp_gt_i32_e64 s[60:61], 26, v172
	v_cmp_gt_i32_e64 s[62:63], 27, v172
	v_cmp_gt_i32_e64 s[58:59], 25, v172
	s_and_b64 s[60:61], s[62:63], s[60:61]
	v_cmp_gt_i32_e64 s[56:57], 24, v172
	s_and_b64 s[58:59], s[60:61], s[58:59]
	v_cmp_gt_i32_e64 s[54:55], 19, v172
	s_and_b64 s[56:57], s[58:59], s[56:57]
	v_cmp_gt_i32_e64 s[52:53], 18, v172
	s_and_b64 s[54:55], s[56:57], s[54:55]
	v_cmp_gt_i32_e64 s[50:51], 17, v172
	s_and_b64 s[52:53], s[54:55], s[52:53]
	v_cmp_gt_i32_e64 s[48:49], 16, v172
	s_and_b64 s[50:51], s[52:53], s[50:51]
	v_cmp_gt_i32_e64 s[46:47], 11, v172
	s_and_b64 s[48:49], s[50:51], s[48:49]
	v_cmp_gt_i32_e64 s[44:45], 10, v172
	s_and_b64 s[46:47], s[48:49], s[46:47]
	v_cmp_gt_i32_e64 s[42:43], 9, v172
	s_and_b64 s[44:45], s[46:47], s[44:45]
	v_cmp_gt_i32_e64 s[40:41], 8, v172
	s_and_b64 s[42:43], s[44:45], s[42:43]
	v_cmp_gt_i32_e64 s[38:39], 3, v172
	s_and_b64 s[40:41], s[42:43], s[40:41]
	v_cmp_gt_i32_e64 s[36:37], 2, v172
	s_and_b64 s[38:39], s[40:41], s[38:39]
	v_cmp_gt_i32_e64 s[34:35], 1, v172
	s_and_b64 s[36:37], s[38:39], s[36:37]
	v_cmp_gt_i32_e64 s[30:31], 0, v172
	s_and_b64 s[34:35], s[36:37], s[34:35]
	s_and_b64 s[30:31], s[34:35], s[30:31]
	v_cmp_gt_i32_e64 s[28:29], 58, v172
	v_cndmask_b32_e64 v66, v66, v243, s[30:31]
	v_cmp_gt_i32_e64 s[30:31], 59, v172
	v_cmp_gt_i32_e64 s[26:27], 57, v172
	s_and_b64 s[28:29], s[30:31], s[28:29]
	v_cmp_gt_i32_e64 s[24:25], 56, v172
	s_and_b64 s[26:27], s[28:29], s[26:27]
	v_cmp_gt_i32_e64 s[22:23], 51, v172
	s_and_b64 s[24:25], s[26:27], s[24:25]
	v_cmp_gt_i32_e64 s[20:21], 50, v172
	s_and_b64 s[22:23], s[24:25], s[22:23]
	v_cmp_gt_i32_e64 s[18:19], 49, v172
	s_and_b64 s[20:21], s[22:23], s[20:21]
	v_cmp_gt_i32_e64 s[16:17], 48, v172
	s_and_b64 s[18:19], s[20:21], s[18:19]
	v_cmp_gt_i32_e64 s[14:15], 43, v172
	s_and_b64 s[16:17], s[18:19], s[16:17]
	v_cmp_gt_i32_e64 s[12:13], 42, v172
	s_and_b64 s[14:15], s[16:17], s[14:15]
	v_cmp_gt_i32_e64 s[10:11], 41, v172
	s_and_b64 s[12:13], s[14:15], s[12:13]
	v_cmp_gt_i32_e64 s[8:9], 40, v172
	s_and_b64 s[10:11], s[12:13], s[10:11]
	v_cmp_gt_i32_e64 s[6:7], 35, v172
	s_and_b64 s[8:9], s[10:11], s[8:9]
	v_cmp_gt_i32_e64 s[4:5], 34, v172
	s_and_b64 s[6:7], s[8:9], s[6:7]
	v_cmp_gt_i32_e64 s[2:3], 33, v172
	s_and_b64 s[4:5], s[6:7], s[4:5]
	v_cmp_gt_i32_e32 vcc, 32, v172
	s_and_b64 s[2:3], s[4:5], s[2:3]
	v_cndmask_b32_e64 v80, v80, v243, s[60:61]
	s_mov_b32 s60, 2.0
	v_cndmask_b32_e64 v79, v79, v243, s[58:59]
	s_mov_b32 s58, 0x41800000
	s_and_b64 vcc, s[2:3], vcc
	v_cndmask_b32_e64 v81, v81, v243, s[62:63]
	s_mov_b32 s61, 0x40400000
	s_mov_b32 s59, 0x41880000
	v_cndmask_b32_e64 v78, v78, v243, s[56:57]
	v_cndmask_b32_e64 v77, v77, v243, s[54:55]
	v_cndmask_b32_e64 v76, v76, v243, s[52:53]
	v_cndmask_b32_e64 v75, v75, v243, s[50:51]
	v_cndmask_b32_e64 v74, v74, v243, s[48:49]
	v_cndmask_b32_e64 v73, v73, v243, s[46:47]
	v_cndmask_b32_e64 v72, v72, v243, s[44:45]
	v_cndmask_b32_e64 v71, v71, v243, s[42:43]
	v_cndmask_b32_e64 v70, v70, v243, s[40:41]
	v_cndmask_b32_e64 v69, v69, v243, s[38:39]
	v_cndmask_b32_e64 v68, v68, v243, s[36:37]
	v_cndmask_b32_e64 v67, v67, v243, s[34:35]
	v_cndmask_b32_e64 v97, v97, v243, s[30:31]
	v_cndmask_b32_e64 v96, v96, v243, s[28:29]
	v_cndmask_b32_e64 v95, v95, v243, s[26:27]
	v_cndmask_b32_e64 v94, v94, v243, s[24:25]
	v_cndmask_b32_e64 v93, v93, v243, s[22:23]
	v_cndmask_b32_e64 v92, v92, v243, s[20:21]
	v_cndmask_b32_e64 v91, v91, v243, s[18:19]
	v_cndmask_b32_e64 v90, v90, v243, s[16:17]
	v_cndmask_b32_e64 v89, v89, v243, s[14:15]
	v_cndmask_b32_e64 v88, v88, v243, s[12:13]
	v_cndmask_b32_e64 v87, v87, v243, s[10:11]
	v_cndmask_b32_e64 v86, v86, v243, s[8:9]
	v_cndmask_b32_e64 v85, v85, v243, s[6:7]
	v_cndmask_b32_e64 v84, v84, v243, s[4:5]
	v_cndmask_b32_e64 v83, v83, v243, s[2:3]
	v_cndmask_b32_e32 v82, v82, v243, vcc

.LBB0_1354:
	v_cvt_f32_i32_e32 v130, v226
	v_mul_f32_e64 v0, -v190, v130
	s_mov_b32 s2, 0x41900000
	s_mov_b32 s3, 0x41980000
	v_fma_f32 v140, v196, s2, v0
	v_fma_f32 v141, v197, s3, v0
	s_mov_b32 s2, 0x41c00000
	s_mov_b32 s3, 0x41c80000
	v_fma_f32 v142, v196, s2, v0
	v_fma_f32 v143, v197, s3, v0
	s_mov_b32 s2, 0x41d00000
	s_mov_b32 s3, 0x41d80000
	v_fma_f32 v144, v196, s2, v0
	v_fma_f32 v145, v197, s3, v0
	s_mov_b32 s2, 0x42000000
	v_fma_f32 v131, -v190, v130, v190
	v_mov_b32_e32 v130, v0
	s_mov_b32 s3, 0x42040000
	v_fmac_f32_e32 v130, 0, v190
	v_fma_f32 v132, v196, s60, v0
	v_fma_f32 v133, v197, s61, v0
	v_fma_f32 v134, v196, s74, v0
	v_fma_f32 v135, v197, s75, v0
	v_fma_f32 v136, v196, s62, v0
	v_fma_f32 v137, v197, s63, v0
	v_fma_f32 v138, v196, s58, v0
	v_fma_f32 v139, v197, s59, v0
	v_fma_f32 v160, v196, s68, v0
	v_fma_f32 v161, v197, s69, v0
	v_fma_f32 v158, v196, s96, v0
	v_fma_f32 v159, v197, s97, v0
	v_fma_f32 v156, v196, s94, v0
	v_fma_f32 v157, v197, s95, v0
	v_fma_f32 v154, v196, s92, v0
	v_fma_f32 v155, v197, s93, v0
	v_fma_f32 v152, v196, s90, v0
	v_fma_f32 v153, v197, s91, v0
	v_fma_f32 v150, v196, s88, v0
	v_fma_f32 v151, v197, s89, v0
	v_fma_f32 v148, v196, s86, v0
	v_fma_f32 v149, v197, s87, v0
	v_fma_f32 v146, v192, s2, v0
	v_fma_f32 v147, v193, s3, v0
	s_setprio 1
	ds_read_b128 v[186:189], v205
	ds_read_b128 v[206:209], v205 offset:1024
	ds_read_b128 v[182:185], v224
	ds_read_b128 v[238:241], v224 offset:8192
	ds_read_b128 v[244:247], v223
	ds_read_b128 v[250:253], v223 offset:8192
	s_waitcnt lgkmcnt(3)
	v_mfma_f32_32x32x16_bf16 v[130:145], v[182:185], v[178:181], v[130:145]
	ds_read_b128 v[182:185], v222
	s_waitcnt lgkmcnt(3)
	v_mfma_f32_32x32x16_bf16 v[146:161], v[238:241], v[178:181], v[146:161]
	ds_read_b128 v[238:241], v222 offset:8192
	s_waitcnt lgkmcnt(3)
	v_mfma_f32_32x32x16_bf16 v[130:145], v[244:247], v[170:173], v[130:145]
	ds_read_b128 v[244:247], v221
	s_waitcnt lgkmcnt(3)
	v_mfma_f32_32x32x16_bf16 v[146:161], v[250:253], v[170:173], v[146:161]
	ds_read_b128 v[250:253], v221 offset:8192
	s_waitcnt lgkmcnt(3)
	v_mfma_f32_32x32x16_bf16 v[130:145], v[182:185], v[166:169], v[130:145]
	ds_read_b128 v[182:185], v224 offset:128
	s_waitcnt lgkmcnt(3)
	v_mfma_f32_32x32x16_bf16 v[146:161], v[238:241], v[166:169], v[146:161]
	ds_read_b128 v[238:241], v224 offset:8320
	s_waitcnt lgkmcnt(3)
	v_mfma_f32_32x32x16_bf16 v[130:145], v[244:247], v[162:165], v[130:145]
	ds_read_b128 v[244:247], v223 offset:128
	s_waitcnt lgkmcnt(3)
	v_mfma_f32_32x32x16_bf16 v[146:161], v[250:253], v[162:165], v[146:161]
	ds_read_b128 v[250:253], v223 offset:8320
	s_waitcnt lgkmcnt(3)
	v_mfma_f32_32x32x16_bf16 v[130:145], v[182:185], v[174:177], v[130:145]
	ds_read_b128 v[182:185], v222 offset:128
	s_waitcnt lgkmcnt(3)
	v_mfma_f32_32x32x16_bf16 v[146:161], v[238:241], v[174:177], v[146:161]
	ds_read_b128 v[238:241], v222 offset:8320
	s_waitcnt lgkmcnt(3)
	v_mfma_f32_32x32x16_bf16 v[130:145], v[244:247], v[186:189], v[130:145]
	ds_read_b128 v[244:247], v221 offset:128
	s_waitcnt lgkmcnt(3)
	v_mfma_f32_32x32x16_bf16 v[146:161], v[250:253], v[186:189], v[146:161]
	ds_read_b128 v[250:253], v221 offset:8320
	ds_read_b128 v[186:189], v205 offset:2048
	s_waitcnt lgkmcnt(4)
	v_mfma_f32_32x32x16_bf16 v[130:145], v[182:185], v[206:209], v[130:145]
	s_waitcnt lgkmcnt(3)
	v_mfma_f32_32x32x16_bf16 v[146:161], v[238:241], v[206:209], v[146:161]
	s_waitcnt lgkmcnt(0)
	v_mfma_f32_32x32x16_bf16 v[130:145], v[244:247], v[186:189], v[130:145]
	s_waitcnt lgkmcnt(0)
	v_mfma_f32_32x32x16_bf16 v[146:161], v[250:253], v[186:189], v[146:161]
	s_setprio 0
	s_add_i32 s2, s85, 0xffffff9f
	s_cmp_le_i32 s2, s65
	s_cbranch_scc1 .LBB0_1356
	v_cmp_gt_i32_e64 s[60:61], 26, v226
	v_cmp_gt_i32_e64 s[62:63], 27, v226
	v_cmp_gt_i32_e64 s[58:59], 25, v226
	s_and_b64 s[60:61], s[62:63], s[60:61]
	v_cmp_gt_i32_e64 s[56:57], 24, v226
	s_and_b64 s[58:59], s[60:61], s[58:59]
	v_cmp_gt_i32_e64 s[54:55], 19, v226
	s_and_b64 s[56:57], s[58:59], s[56:57]
	v_cmp_gt_i32_e64 s[52:53], 18, v226
	s_and_b64 s[54:55], s[56:57], s[54:55]
	v_cmp_gt_i32_e64 s[50:51], 17, v226
	s_and_b64 s[52:53], s[54:55], s[52:53]
	v_cmp_gt_i32_e64 s[48:49], 16, v226
	s_and_b64 s[50:51], s[52:53], s[50:51]
	v_cmp_gt_i32_e64 s[46:47], 11, v226
	s_and_b64 s[48:49], s[50:51], s[48:49]
	v_cmp_gt_i32_e64 s[44:45], 10, v226
	s_and_b64 s[46:47], s[48:49], s[46:47]
	v_cmp_gt_i32_e64 s[42:43], 9, v226
	s_and_b64 s[44:45], s[46:47], s[44:45]
	v_cmp_gt_i32_e64 s[40:41], 8, v226
	s_and_b64 s[42:43], s[44:45], s[42:43]
	v_cmp_gt_i32_e64 s[38:39], 3, v226
	s_and_b64 s[40:41], s[42:43], s[40:41]
	v_cmp_gt_i32_e64 s[36:37], 2, v226
	s_and_b64 s[38:39], s[40:41], s[38:39]
	v_cmp_gt_i32_e64 s[34:35], 1, v226
	s_and_b64 s[36:37], s[38:39], s[36:37]
	v_cmp_gt_i32_e64 s[30:31], 0, v226
	s_and_b64 s[34:35], s[36:37], s[34:35]
	s_and_b64 s[30:31], s[34:35], s[30:31]
	v_cmp_gt_i32_e64 s[28:29], 58, v226
	v_cndmask_b32_e64 v130, v130, v243, s[30:31]
	v_cmp_gt_i32_e64 s[30:31], 59, v226
	v_cmp_gt_i32_e64 s[26:27], 57, v226
	s_and_b64 s[28:29], s[30:31], s[28:29]
	v_cmp_gt_i32_e64 s[24:25], 56, v226
	s_and_b64 s[26:27], s[28:29], s[26:27]
	v_cmp_gt_i32_e64 s[22:23], 51, v226
	s_and_b64 s[24:25], s[26:27], s[24:25]
	v_cmp_gt_i32_e64 s[20:21], 50, v226
	s_and_b64 s[22:23], s[24:25], s[22:23]
	v_cmp_gt_i32_e64 s[18:19], 49, v226
	s_and_b64 s[20:21], s[22:23], s[20:21]
	v_cmp_gt_i32_e64 s[16:17], 48, v226
	s_and_b64 s[18:19], s[20:21], s[18:19]
	v_cmp_gt_i32_e64 s[14:15], 43, v226
	s_and_b64 s[16:17], s[18:19], s[16:17]
	v_cmp_gt_i32_e64 s[12:13], 42, v226
	s_and_b64 s[14:15], s[16:17], s[14:15]
	v_cmp_gt_i32_e64 s[10:11], 41, v226
	s_and_b64 s[12:13], s[14:15], s[12:13]
	v_cmp_gt_i32_e64 s[8:9], 40, v226
	s_and_b64 s[10:11], s[12:13], s[10:11]
	v_cmp_gt_i32_e64 s[6:7], 35, v226
	s_and_b64 s[8:9], s[10:11], s[8:9]
	v_cmp_gt_i32_e64 s[4:5], 34, v226
	s_and_b64 s[6:7], s[8:9], s[6:7]
	v_cmp_gt_i32_e64 s[2:3], 33, v226
	s_and_b64 s[4:5], s[6:7], s[4:5]
	v_cmp_gt_i32_e32 vcc, 32, v226
	s_and_b64 s[2:3], s[4:5], s[2:3]
	v_cndmask_b32_e64 v145, v145, v243, s[62:63]
	s_mov_b32 s62, 0x41200000
	v_cndmask_b32_e64 v144, v144, v243, s[60:61]
	s_mov_b32 s60, 2.0
	v_cndmask_b32_e64 v143, v143, v243, s[58:59]
	s_mov_b32 s58, 0x41800000
	s_and_b64 vcc, s[2:3], vcc
	s_mov_b32 s63, 0x41300000
	s_mov_b32 s61, 0x40400000
	s_mov_b32 s59, 0x41880000
	v_cndmask_b32_e64 v142, v142, v243, s[56:57]
	v_cndmask_b32_e64 v141, v141, v243, s[54:55]
	v_cndmask_b32_e64 v140, v140, v243, s[52:53]
	v_cndmask_b32_e64 v139, v139, v243, s[50:51]
	v_cndmask_b32_e64 v138, v138, v243, s[48:49]
	v_cndmask_b32_e64 v137, v137, v243, s[46:47]
	v_cndmask_b32_e64 v136, v136, v243, s[44:45]
	v_cndmask_b32_e64 v135, v135, v243, s[42:43]
	v_cndmask_b32_e64 v134, v134, v243, s[40:41]
	v_cndmask_b32_e64 v133, v133, v243, s[38:39]
	v_cndmask_b32_e64 v132, v132, v243, s[36:37]
	v_cndmask_b32_e64 v131, v131, v243, s[34:35]
	v_cndmask_b32_e64 v161, v161, v243, s[30:31]
	v_cndmask_b32_e64 v160, v160, v243, s[28:29]
	v_cndmask_b32_e64 v159, v159, v243, s[26:27]
	v_cndmask_b32_e64 v158, v158, v243, s[24:25]
	v_cndmask_b32_e64 v157, v157, v243, s[22:23]
	v_cndmask_b32_e64 v156, v156, v243, s[20:21]
	v_cndmask_b32_e64 v155, v155, v243, s[18:19]
	v_cndmask_b32_e64 v154, v154, v243, s[16:17]
	v_cndmask_b32_e64 v153, v153, v243, s[14:15]
	v_cndmask_b32_e64 v152, v152, v243, s[12:13]
	v_cndmask_b32_e64 v151, v151, v243, s[10:11]
	v_cndmask_b32_e64 v150, v150, v243, s[8:9]
	v_cndmask_b32_e64 v149, v149, v243, s[6:7]
	v_cndmask_b32_e64 v148, v148, v243, s[4:5]
	v_cndmask_b32_e64 v147, v147, v243, s[2:3]
	v_cndmask_b32_e32 v146, v146, v243, vcc

.LBB0_1360:
	v_lshl_add_u64 v[146:147], s[76:77], 0, v[194:195]
	v_add_co_u32_e32 v150, vcc, 0xc4000, v146
	v_lshl_add_u64 v[182:183], s[72:73], 0, v[194:195]
	s_nop 0
	v_addc_co_u32_e32 v151, vcc, 0, v147, vcc
	v_add_co_u32_e32 v154, vcc, 0x126000, v146
	s_nop 1
	v_addc_co_u32_e32 v155, vcc, 0, v147, vcc
	v_add_co_u32_e32 v184, vcc, 0xc4000, v182
	global_load_dwordx4 v[146:149], v[150:151], off
	s_nop 0
	global_load_dwordx4 v[150:153], v[150:151], off offset:256
	s_nop 0
	global_load_dwordx4 v[158:161], v[154:155], off
	s_nop 0
	global_load_dwordx4 v[154:157], v[154:155], off offset:256
	v_addc_co_u32_e32 v185, vcc, 0, v183, vcc
	v_add_co_u32_e32 v186, vcc, 0x126000, v182
	s_nop 1
	v_addc_co_u32_e32 v187, vcc, 0, v183, vcc
	global_load_dwordx4 v[182:185], v[184:185], off
	s_nop 0
	global_load_dwordx4 v[186:189], v[186:187], off
	s_setprio 1
	ds_read_b64_tr_b16 v[238:239], v213 offset:0
	ds_read_b64_tr_b16 v[240:241], v213 offset:0x1000
	ds_read_b64_tr_b16 v[244:245], v213 offset:0x2000
	ds_read_b64_tr_b16 v[246:247], v213 offset:0x3000
	ds_read_b64_tr_b16 v[250:251], v213 offset:0x4000
	ds_read_b64_tr_b16 v[252:253], v213 offset:0x5000
	ds_read_b64_tr_b16 v[206:207], v213 offset:0x6000
	ds_read_b64_tr_b16 v[208:209], v213 offset:0x7000
	s_waitcnt lgkmcnt(0)
	s_nop 0
	v_mfma_f32_32x32x16_bf16 v[114:129], v[130:133], v[238:241], v[114:129]
	v_mfma_f32_32x32x16_bf16 v[114:129], v[134:137], v[244:247], v[114:129]
	v_mfma_f32_32x32x16_bf16 v[114:129], v[138:141], v[250:253], v[114:129]
	v_mfma_f32_32x32x16_bf16 v[114:129], v[142:145], v[206:209], v[114:129]
	ds_read_b64_tr_b16 v[206:207], v213 offset:0x200
	ds_read_b64_tr_b16 v[208:209], v213 offset:0x1200
	ds_read_b64_tr_b16 v[238:239], v213 offset:0x2200
	ds_read_b64_tr_b16 v[240:241], v213 offset:0x3200
	ds_read_b64_tr_b16 v[244:245], v213 offset:0x4200
	ds_read_b64_tr_b16 v[246:247], v213 offset:0x5200
	ds_read_b64_tr_b16 v[250:251], v213 offset:0x6200
	ds_read_b64_tr_b16 v[252:253], v213 offset:0x7200
	s_waitcnt lgkmcnt(0)
	s_nop 0
	v_mfma_f32_32x32x16_bf16 v[98:113], v[130:133], v[206:209], v[98:113]
	ds_read_b64_tr_b16 v[206:207], v213 offset:0x400
	ds_read_b64_tr_b16 v[208:209], v213 offset:0x1400
	v_mfma_f32_32x32x16_bf16 v[98:113], v[134:137], v[238:241], v[98:113]
	ds_read_b64_tr_b16 v[238:239], v213 offset:0x2400
	ds_read_b64_tr_b16 v[240:241], v213 offset:0x3400
	v_mfma_f32_32x32x16_bf16 v[98:113], v[138:141], v[244:247], v[98:113]
	ds_read_b64_tr_b16 v[244:245], v213 offset:0x4400
	ds_read_b64_tr_b16 v[246:247], v213 offset:0x5400
	v_mfma_f32_32x32x16_bf16 v[98:113], v[142:145], v[250:253], v[98:113]
	ds_read_b64_tr_b16 v[250:251], v213 offset:0x6400
	ds_read_b64_tr_b16 v[252:253], v213 offset:0x7400
	s_waitcnt lgkmcnt(0)
	v_mfma_f32_32x32x16_bf16 v[82:97], v[130:133], v[206:209], v[82:97]
	ds_read_b64_tr_b16 v[206:207], v213 offset:0x600
	ds_read_b64_tr_b16 v[208:209], v213 offset:0x1600
	v_mfma_f32_32x32x16_bf16 v[82:97], v[134:137], v[238:241], v[82:97]
	ds_read_b64_tr_b16 v[238:239], v213 offset:0x2600
	ds_read_b64_tr_b16 v[240:241], v213 offset:0x3600
	v_mfma_f32_32x32x16_bf16 v[82:97], v[138:141], v[244:247], v[82:97]
	ds_read_b64_tr_b16 v[244:245], v213 offset:0x4600
	ds_read_b64_tr_b16 v[246:247], v213 offset:0x5600
	v_mfma_f32_32x32x16_bf16 v[82:97], v[142:145], v[250:253], v[82:97]
	ds_read_b64_tr_b16 v[250:251], v213 offset:0x6600
	ds_read_b64_tr_b16 v[252:253], v213 offset:0x7600
	s_waitcnt lgkmcnt(0)
	v_mfma_f32_32x32x16_bf16 v[66:81], v[130:133], v[206:209], v[66:81]
	ds_read_b64_tr_b16 v[206:207], v213 offset:0x800
	ds_read_b64_tr_b16 v[208:209], v213 offset:0x1800
	v_mfma_f32_32x32x16_bf16 v[66:81], v[134:137], v[238:241], v[66:81]
	ds_read_b64_tr_b16 v[238:239], v213 offset:0x2800
	ds_read_b64_tr_b16 v[240:241], v213 offset:0x3800
	v_mfma_f32_32x32x16_bf16 v[66:81], v[138:141], v[244:247], v[66:81]
	ds_read_b64_tr_b16 v[244:245], v213 offset:0x4800
	ds_read_b64_tr_b16 v[246:247], v213 offset:0x5800
	v_mfma_f32_32x32x16_bf16 v[66:81], v[142:145], v[250:253], v[66:81]
	ds_read_b64_tr_b16 v[250:251], v213 offset:0x6800
	ds_read_b64_tr_b16 v[252:253], v213 offset:0x7800
	s_waitcnt lgkmcnt(0)
	v_mfma_f32_32x32x16_bf16 v[50:65], v[130:133], v[206:209], v[50:65]
	ds_read_b64_tr_b16 v[206:207], v213 offset:0xa00
	ds_read_b64_tr_b16 v[208:209], v213 offset:0x1a00
	v_mfma_f32_32x32x16_bf16 v[50:65], v[134:137], v[238:241], v[50:65]
	ds_read_b64_tr_b16 v[238:239], v213 offset:0x2a00
	ds_read_b64_tr_b16 v[240:241], v213 offset:0x3a00
	v_mfma_f32_32x32x16_bf16 v[50:65], v[138:141], v[244:247], v[50:65]
	ds_read_b64_tr_b16 v[244:245], v213 offset:0x4a00
	ds_read_b64_tr_b16 v[246:247], v213 offset:0x5a00
	v_mfma_f32_32x32x16_bf16 v[50:65], v[142:145], v[250:253], v[50:65]
	ds_read_b64_tr_b16 v[250:251], v213 offset:0x6a00
	ds_read_b64_tr_b16 v[252:253], v213 offset:0x7a00
	s_waitcnt lgkmcnt(0)
	v_mfma_f32_32x32x16_bf16 v[34:49], v[130:133], v[206:209], v[34:49]
	ds_read_b64_tr_b16 v[206:207], v213 offset:0xc00
	ds_read_b64_tr_b16 v[208:209], v213 offset:0x1c00
	v_mfma_f32_32x32x16_bf16 v[34:49], v[134:137], v[238:241], v[34:49]
	ds_read_b64_tr_b16 v[238:239], v213 offset:0x2c00
	ds_read_b64_tr_b16 v[240:241], v213 offset:0x3c00
	v_mfma_f32_32x32x16_bf16 v[34:49], v[138:141], v[244:247], v[34:49]
	ds_read_b64_tr_b16 v[244:245], v213 offset:0x4c00
	ds_read_b64_tr_b16 v[246:247], v213 offset:0x5c00
	v_mfma_f32_32x32x16_bf16 v[34:49], v[142:145], v[250:253], v[34:49]
	ds_read_b64_tr_b16 v[250:251], v213 offset:0x6c00
	ds_read_b64_tr_b16 v[252:253], v213 offset:0x7c00
	s_waitcnt lgkmcnt(0)
	v_mfma_f32_32x32x16_bf16 v[18:33], v[130:133], v[206:209], v[18:33]
	ds_read_b64_tr_b16 v[206:207], v213 offset:0xe00
	ds_read_b64_tr_b16 v[208:209], v213 offset:0x1e00
	v_mfma_f32_32x32x16_bf16 v[18:33], v[134:137], v[238:241], v[18:33]
	ds_read_b64_tr_b16 v[238:239], v213 offset:0x2e00
	ds_read_b64_tr_b16 v[240:241], v213 offset:0x3e00
	v_mfma_f32_32x32x16_bf16 v[18:33], v[138:141], v[244:247], v[18:33]
	ds_read_b64_tr_b16 v[244:245], v213 offset:0x4e00
	ds_read_b64_tr_b16 v[246:247], v213 offset:0x5e00
	v_mfma_f32_32x32x16_bf16 v[18:33], v[142:145], v[250:253], v[18:33]
	ds_read_b64_tr_b16 v[250:251], v213 offset:0x6e00
	ds_read_b64_tr_b16 v[252:253], v213 offset:0x7e00
	s_waitcnt lgkmcnt(0)
	v_mfma_f32_32x32x16_bf16 v[2:17], v[130:133], v[206:209], v[2:17]
	v_mfma_f32_32x32x16_bf16 v[2:17], v[134:137], v[238:241], v[2:17]
	v_mfma_f32_32x32x16_bf16 v[2:17], v[138:141], v[244:247], v[2:17]
	v_mfma_f32_32x32x16_bf16 v[2:17], v[142:145], v[250:253], v[2:17]
	s_setprio 0
	v_add_u32_e32 v227, 0x14000, v225
	s_waitcnt vmcnt(0)
	s_waitcnt vmcnt(1)
	ds_write_b128 v227, v[182:185]
	s_waitcnt vmcnt(0)
	ds_write_b128 v227, v[186:189] offset:8192
	ds_write_b128 v220, v[146:149] offset:32768
	ds_write_b128 v220, v[158:161] offset:49152
	ds_write_b128 v220, v[150:153] offset:34816
	ds_write_b128 v220, v[154:157] offset:51200
	v_subrev_u32_e32 v182, 64, v226
	v_cvt_f32_i32_e32 v130, v182
	s_waitcnt lgkmcnt(0)
	s_barrier
	v_mul_f32_e64 v146, -v190, v130
	s_mov_b32 s2, 0x41900000
	s_mov_b32 s3, 0x41980000
	v_fma_f32 v140, v196, s2, v146
	v_fma_f32 v141, v197, s3, v146
	s_mov_b32 s2, 0x41c00000
	s_mov_b32 s3, 0x41c80000
	v_fma_f32 v142, v196, s2, v146
	v_fma_f32 v143, v197, s3, v146
	s_mov_b32 s2, 0x41d00000
	s_mov_b32 s3, 0x41d80000
	v_fma_f32 v144, v196, s2, v146
	v_fma_f32 v145, v197, s3, v146
	s_mov_b32 s2, 0x42000000
	v_fma_f32 v131, -v190, v130, v190
	v_mov_b32_e32 v130, v146
	v_mov_b32_e32 v191, v190
	s_mov_b32 s3, 0x42040000
	v_fmac_f32_e32 v130, 0, v190
	v_fma_f32 v132, v196, s60, v146
	v_fma_f32 v133, v197, s61, v146
	v_fma_f32 v134, v196, s74, v146
	v_fma_f32 v135, v197, s75, v146
	v_fma_f32 v136, v196, s62, v146
	v_fma_f32 v137, v197, s63, v146
	v_fma_f32 v138, v196, s58, v146
	v_fma_f32 v139, v197, s59, v146
	v_fma_f32 v160, v190, s68, v146
	v_fma_f32 v161, v191, s69, v146
	v_fma_f32 v158, v190, s96, v146
	v_fma_f32 v159, v191, s97, v146
	v_fma_f32 v156, v190, s94, v146
	v_fma_f32 v157, v191, s95, v146
	v_fma_f32 v154, v190, s92, v146
	v_fma_f32 v155, v191, s93, v146
	v_fma_f32 v152, v190, s90, v146
	v_fma_f32 v153, v191, s91, v146
	v_fma_f32 v150, v190, s88, v146
	v_fma_f32 v151, v191, s89, v146
	v_fma_f32 v148, v190, s86, v146
	v_fma_f32 v149, v191, s87, v146
	v_fma_f32 v147, v193, s3, v146
	v_fma_f32 v146, v192, s2, v146
	s_setprio 1
	ds_read_b128 v[206:209], v205
	ds_read_b128 v[250:253], v205 offset:1024
	ds_read_b128 v[184:187], v218
	ds_read_b128 v[238:241], v218 offset:8192
	ds_read_b128 v[244:247], v217
	s_waitcnt lgkmcnt(2)
	v_mfma_f32_32x32x16_bf16 v[130:145], v[184:187], v[178:181], v[130:145]
	ds_read_b128 v[184:187], v217 offset:8192
	s_waitcnt lgkmcnt(2)
	v_mfma_f32_32x32x16_bf16 v[146:161], v[238:241], v[178:181], v[146:161]
	ds_read_b128 v[238:241], v216
	s_waitcnt lgkmcnt(2)
	v_mfma_f32_32x32x16_bf16 v[130:145], v[244:247], v[170:173], v[130:145]
	ds_read_b128 v[244:247], v216 offset:8192
	s_waitcnt lgkmcnt(2)
	v_mfma_f32_32x32x16_bf16 v[146:161], v[184:187], v[170:173], v[146:161]
	ds_read_b128 v[184:187], v215
	s_waitcnt lgkmcnt(2)
	v_mfma_f32_32x32x16_bf16 v[130:145], v[238:241], v[166:169], v[130:145]
	ds_read_b128 v[238:241], v215 offset:8192
	s_waitcnt lgkmcnt(2)
	v_mfma_f32_32x32x16_bf16 v[146:161], v[244:247], v[166:169], v[146:161]
	ds_read_b128 v[244:247], v218 offset:128
	s_waitcnt lgkmcnt(2)
	v_mfma_f32_32x32x16_bf16 v[130:145], v[184:187], v[162:165], v[130:145]
	ds_read_b128 v[184:187], v218 offset:8320
	s_waitcnt lgkmcnt(2)
	v_mfma_f32_32x32x16_bf16 v[146:161], v[238:241], v[162:165], v[146:161]
	ds_read_b128 v[238:241], v217 offset:128
	s_waitcnt lgkmcnt(2)
	v_mfma_f32_32x32x16_bf16 v[130:145], v[244:247], v[174:177], v[130:145]
	ds_read_b128 v[244:247], v217 offset:8320
	s_waitcnt lgkmcnt(2)
	v_mfma_f32_32x32x16_bf16 v[146:161], v[184:187], v[174:177], v[146:161]
	ds_read_b128 v[184:187], v216 offset:128
	s_waitcnt lgkmcnt(2)
	v_mfma_f32_32x32x16_bf16 v[130:145], v[238:241], v[206:209], v[130:145]
	ds_read_b128 v[238:241], v216 offset:8320
	s_waitcnt lgkmcnt(2)
	v_mfma_f32_32x32x16_bf16 v[146:161], v[244:247], v[206:209], v[146:161]
	ds_read_b128 v[244:247], v215 offset:128
	ds_read_b128 v[206:209], v205 offset:2048
	s_waitcnt lgkmcnt(3)
	v_mfma_f32_32x32x16_bf16 v[130:145], v[184:187], v[250:253], v[130:145]
	ds_read_b128 v[184:187], v215 offset:8320
	s_waitcnt lgkmcnt(3)
	v_mfma_f32_32x32x16_bf16 v[146:161], v[238:241], v[250:253], v[146:161]
	s_waitcnt lgkmcnt(1)
	v_mfma_f32_32x32x16_bf16 v[130:145], v[244:247], v[206:209], v[130:145]
	s_waitcnt lgkmcnt(0)
	v_mfma_f32_32x32x16_bf16 v[146:161], v[184:187], v[206:209], v[146:161]
	s_setprio 0
	s_sub_i32 s2, s85, 33
	s_cmp_le_i32 s2, s65
	s_cbranch_scc1 .LBB0_1362
	v_cmp_gt_i32_e64 s[60:61], 26, v182
	v_cmp_gt_i32_e64 s[62:63], 27, v182
	v_cmp_gt_i32_e64 s[58:59], 25, v182
	s_and_b64 s[60:61], s[62:63], s[60:61]
	v_cmp_gt_i32_e64 s[56:57], 24, v182
	s_and_b64 s[58:59], s[60:61], s[58:59]
	v_cmp_gt_i32_e64 s[54:55], 19, v182
	s_and_b64 s[56:57], s[58:59], s[56:57]
	v_cmp_gt_i32_e64 s[52:53], 18, v182
	s_and_b64 s[54:55], s[56:57], s[54:55]
	v_cmp_gt_i32_e64 s[50:51], 17, v182
	s_and_b64 s[52:53], s[54:55], s[52:53]
	v_cmp_gt_i32_e64 s[48:49], 16, v182
	s_and_b64 s[50:51], s[52:53], s[50:51]
	v_cmp_gt_i32_e64 s[46:47], 11, v182
	s_and_b64 s[48:49], s[50:51], s[48:49]
	v_cmp_gt_i32_e64 s[44:45], 10, v182
	s_and_b64 s[46:47], s[48:49], s[46:47]
	v_cmp_gt_i32_e64 s[42:43], 9, v182
	s_and_b64 s[44:45], s[46:47], s[44:45]
	v_cmp_gt_i32_e64 s[40:41], 8, v182
	s_and_b64 s[42:43], s[44:45], s[42:43]
	v_cmp_gt_i32_e64 s[38:39], 3, v182
	s_and_b64 s[40:41], s[42:43], s[40:41]
	v_cmp_gt_i32_e64 s[36:37], 2, v182
	s_and_b64 s[38:39], s[40:41], s[38:39]
	v_cmp_gt_i32_e64 s[34:35], 1, v182
	s_and_b64 s[36:37], s[38:39], s[36:37]
	v_cmp_gt_i32_e64 s[30:31], 0, v182
	s_and_b64 s[34:35], s[36:37], s[34:35]
	s_and_b64 s[30:31], s[34:35], s[30:31]
	v_cmp_gt_i32_e64 s[28:29], 58, v182
	v_cndmask_b32_e64 v130, v130, v243, s[30:31]
	v_cmp_gt_i32_e64 s[30:31], 59, v182
	v_cmp_gt_i32_e64 s[26:27], 57, v182
	s_and_b64 s[28:29], s[30:31], s[28:29]
	v_cmp_gt_i32_e64 s[24:25], 56, v182
	s_and_b64 s[26:27], s[28:29], s[26:27]
	v_cmp_gt_i32_e64 s[22:23], 51, v182
	s_and_b64 s[24:25], s[26:27], s[24:25]
	v_cmp_gt_i32_e64 s[20:21], 50, v182
	s_and_b64 s[22:23], s[24:25], s[22:23]
	v_cmp_gt_i32_e64 s[18:19], 49, v182
	s_and_b64 s[20:21], s[22:23], s[20:21]
	v_cmp_gt_i32_e64 s[16:17], 48, v182
	s_and_b64 s[18:19], s[20:21], s[18:19]
	v_cmp_gt_i32_e64 s[14:15], 43, v182
	s_and_b64 s[16:17], s[18:19], s[16:17]
	v_cmp_gt_i32_e64 s[12:13], 42, v182
	s_and_b64 s[14:15], s[16:17], s[14:15]
	v_cmp_gt_i32_e64 s[10:11], 41, v182
	s_and_b64 s[12:13], s[14:15], s[12:13]
	v_cmp_gt_i32_e64 s[8:9], 40, v182
	s_and_b64 s[10:11], s[12:13], s[10:11]
	v_cmp_gt_i32_e64 s[6:7], 35, v182
	s_and_b64 s[8:9], s[10:11], s[8:9]
	v_cmp_gt_i32_e64 s[4:5], 34, v182
	s_and_b64 s[6:7], s[8:9], s[6:7]
	v_cmp_gt_i32_e64 s[2:3], 33, v182
	s_and_b64 s[4:5], s[6:7], s[4:5]
	v_cmp_gt_i32_e32 vcc, 32, v182
	s_and_b64 s[2:3], s[4:5], s[2:3]
	v_cndmask_b32_e64 v145, v145, v243, s[62:63]
	s_mov_b32 s62, 0x41200000
	v_cndmask_b32_e64 v144, v144, v243, s[60:61]
	s_mov_b32 s60, 2.0
	v_cndmask_b32_e64 v143, v143, v243, s[58:59]
	s_mov_b32 s58, 0x41800000
	s_and_b64 vcc, s[2:3], vcc
	s_mov_b32 s63, 0x41300000
	s_mov_b32 s61, 0x40400000
	s_mov_b32 s59, 0x41880000
	v_cndmask_b32_e64 v142, v142, v243, s[56:57]
	v_cndmask_b32_e64 v141, v141, v243, s[54:55]
	v_cndmask_b32_e64 v140, v140, v243, s[52:53]
	v_cndmask_b32_e64 v139, v139, v243, s[50:51]
	v_cndmask_b32_e64 v138, v138, v243, s[48:49]
	v_cndmask_b32_e64 v137, v137, v243, s[46:47]
	v_cndmask_b32_e64 v136, v136, v243, s[44:45]
	v_cndmask_b32_e64 v135, v135, v243, s[42:43]
	v_cndmask_b32_e64 v134, v134, v243, s[40:41]
	v_cndmask_b32_e64 v133, v133, v243, s[38:39]
	v_cndmask_b32_e64 v132, v132, v243, s[36:37]
	v_cndmask_b32_e64 v131, v131, v243, s[34:35]
	v_cndmask_b32_e64 v161, v161, v243, s[30:31]
	v_cndmask_b32_e64 v160, v160, v243, s[28:29]
	v_cndmask_b32_e64 v159, v159, v243, s[26:27]
	v_cndmask_b32_e64 v158, v158, v243, s[24:25]
	v_cndmask_b32_e64 v157, v157, v243, s[22:23]
	v_cndmask_b32_e64 v156, v156, v243, s[20:21]
	v_cndmask_b32_e64 v155, v155, v243, s[18:19]
	v_cndmask_b32_e64 v154, v154, v243, s[16:17]
	v_cndmask_b32_e64 v153, v153, v243, s[14:15]
	v_cndmask_b32_e64 v152, v152, v243, s[12:13]
	v_cndmask_b32_e64 v151, v151, v243, s[10:11]
	v_cndmask_b32_e64 v150, v150, v243, s[8:9]
	v_cndmask_b32_e64 v149, v149, v243, s[6:7]
	v_cndmask_b32_e64 v148, v148, v243, s[4:5]
	v_cndmask_b32_e64 v147, v147, v243, s[2:3]
	v_cndmask_b32_e32 v146, v146, v243, vcc

.Lmk_a2:
	s_mov_b32 s2, 0x41900000
	s_mov_b32 s3, 0x41980000
	v_fma_f32 v140, v196, s2, v146
	v_fma_f32 v141, v197, s3, v146
	s_mov_b32 s2, 0x41c00000
	s_mov_b32 s3, 0x41c80000
	v_fma_f32 v142, v196, s2, v146
	v_fma_f32 v143, v197, s3, v146
	s_mov_b32 s2, 0x41d00000
	s_mov_b32 s3, 0x41d80000
	v_fma_f32 v144, v196, s2, v146
	v_fma_f32 v145, v197, s3, v146
	s_mov_b32 s2, 0x42000000
	v_fma_f32 v131, -v190, v130, v190
	v_mov_b32_e32 v130, v146
	v_mov_b32_e32 v191, v190
	s_mov_b32 s3, 0x42040000
	v_fmac_f32_e32 v130, 0, v190
	v_fma_f32 v132, v196, s60, v146
	v_fma_f32 v133, v197, s61, v146
	v_fma_f32 v134, v196, s74, v146
	v_fma_f32 v135, v197, s75, v146
	v_fma_f32 v136, v196, s62, v146
	v_fma_f32 v137, v197, s63, v146
	v_fma_f32 v138, v196, s58, v146
	v_fma_f32 v139, v197, s59, v146
	v_fma_f32 v160, v190, s68, v146
	v_fma_f32 v161, v191, s69, v146
	v_fma_f32 v158, v190, s96, v146
	v_fma_f32 v159, v191, s97, v146
	v_fma_f32 v156, v190, s94, v146
	v_fma_f32 v157, v191, s95, v146
	v_fma_f32 v154, v190, s92, v146
	v_fma_f32 v155, v191, s93, v146
	v_fma_f32 v152, v190, s90, v146
	v_fma_f32 v153, v191, s91, v146
	v_fma_f32 v150, v190, s88, v146
	v_fma_f32 v151, v191, s89, v146
	v_fma_f32 v148, v190, s86, v146
	v_fma_f32 v149, v191, s87, v146
	v_fma_f32 v147, v193, s3, v146
	v_fma_f32 v146, v192, s2, v146
	s_setprio 1
	ds_read_b128 v[198:201], v205
	ds_read_b128 v[206:209], v205 offset:1024
	ds_read_b128 v[184:187], v224
	ds_read_b128 v[238:241], v224 offset:8192
	ds_read_b128 v[244:247], v223
	ds_read_b128 v[250:253], v223 offset:8192
	s_waitcnt lgkmcnt(3)
	v_mfma_f32_32x32x16_bf16 v[130:145], v[184:187], v[178:181], v[130:145]
	ds_read_b128 v[184:187], v222
	s_waitcnt lgkmcnt(3)
	v_mfma_f32_32x32x16_bf16 v[146:161], v[238:241], v[178:181], v[146:161]
	ds_read_b128 v[238:241], v222 offset:8192
	s_waitcnt lgkmcnt(3)
	v_mfma_f32_32x32x16_bf16 v[130:145], v[244:247], v[170:173], v[130:145]
	ds_read_b128 v[244:247], v221
	s_waitcnt lgkmcnt(3)
	v_mfma_f32_32x32x16_bf16 v[146:161], v[250:253], v[170:173], v[146:161]
	ds_read_b128 v[250:253], v221 offset:8192
	s_waitcnt lgkmcnt(3)
	v_mfma_f32_32x32x16_bf16 v[130:145], v[184:187], v[166:169], v[130:145]
	ds_read_b128 v[184:187], v224 offset:128
	s_waitcnt lgkmcnt(3)
	v_mfma_f32_32x32x16_bf16 v[146:161], v[238:241], v[166:169], v[146:161]
	ds_read_b128 v[238:241], v224 offset:8320
	s_waitcnt lgkmcnt(3)
	v_mfma_f32_32x32x16_bf16 v[130:145], v[244:247], v[162:165], v[130:145]
	ds_read_b128 v[244:247], v223 offset:128
	s_waitcnt lgkmcnt(3)
	v_mfma_f32_32x32x16_bf16 v[146:161], v[250:253], v[162:165], v[146:161]
	ds_read_b128 v[250:253], v223 offset:8320
	s_waitcnt lgkmcnt(3)
	v_mfma_f32_32x32x16_bf16 v[130:145], v[184:187], v[174:177], v[130:145]
	ds_read_b128 v[184:187], v222 offset:128
	s_waitcnt lgkmcnt(3)
	v_mfma_f32_32x32x16_bf16 v[146:161], v[238:241], v[174:177], v[146:161]
	ds_read_b128 v[238:241], v222 offset:8320
	s_waitcnt lgkmcnt(3)
	v_mfma_f32_32x32x16_bf16 v[130:145], v[244:247], v[198:201], v[130:145]
	ds_read_b128 v[244:247], v221 offset:128
	s_waitcnt lgkmcnt(3)
	v_mfma_f32_32x32x16_bf16 v[146:161], v[250:253], v[198:201], v[146:161]
	ds_read_b128 v[250:253], v221 offset:8320
	ds_read_b128 v[198:201], v205 offset:2048
	s_waitcnt lgkmcnt(4)
	v_mfma_f32_32x32x16_bf16 v[130:145], v[184:187], v[206:209], v[130:145]
	s_waitcnt lgkmcnt(3)
	v_mfma_f32_32x32x16_bf16 v[146:161], v[238:241], v[206:209], v[146:161]
	s_waitcnt lgkmcnt(0)
	v_mfma_f32_32x32x16_bf16 v[130:145], v[244:247], v[198:201], v[130:145]
	s_waitcnt lgkmcnt(0)
	v_mfma_f32_32x32x16_bf16 v[146:161], v[250:253], v[198:201], v[146:161]
	s_setprio 0
	s_add_i32 s2, s72, 0xffffffbf
	s_cmp_gt_i32 s2, s65
	s_cbranch_scc0 .LBB0_1367
	v_cmp_gt_i32_e64 s[60:61], 26, v182
	v_cmp_gt_i32_e64 s[62:63], 27, v182
	v_cmp_gt_i32_e64 s[58:59], 25, v182
	s_and_b64 s[60:61], s[62:63], s[60:61]
	v_cmp_gt_i32_e64 s[56:57], 24, v182
	s_and_b64 s[58:59], s[60:61], s[58:59]
	v_cmp_gt_i32_e64 s[54:55], 19, v182
	s_and_b64 s[56:57], s[58:59], s[56:57]
	v_cmp_gt_i32_e64 s[52:53], 18, v182
	s_and_b64 s[54:55], s[56:57], s[54:55]
	v_cmp_gt_i32_e64 s[50:51], 17, v182
	s_and_b64 s[52:53], s[54:55], s[52:53]
	v_cmp_gt_i32_e64 s[48:49], 16, v182
	s_and_b64 s[50:51], s[52:53], s[50:51]
	v_cmp_gt_i32_e64 s[46:47], 11, v182
	s_and_b64 s[48:49], s[50:51], s[48:49]
	v_cmp_gt_i32_e64 s[44:45], 10, v182
	s_and_b64 s[46:47], s[48:49], s[46:47]
	v_cmp_gt_i32_e64 s[42:43], 9, v182
	s_and_b64 s[44:45], s[46:47], s[44:45]
	v_cmp_gt_i32_e64 s[40:41], 8, v182
	s_and_b64 s[42:43], s[44:45], s[42:43]
	v_cmp_gt_i32_e64 s[38:39], 3, v182
	s_and_b64 s[40:41], s[42:43], s[40:41]
	v_cmp_gt_i32_e64 s[36:37], 2, v182
	s_and_b64 s[38:39], s[40:41], s[38:39]
	v_cmp_gt_i32_e64 s[34:35], 1, v182
	s_and_b64 s[36:37], s[38:39], s[36:37]
	v_cmp_gt_i32_e64 s[30:31], 0, v182
	s_and_b64 s[34:35], s[36:37], s[34:35]
	s_and_b64 s[30:31], s[34:35], s[30:31]
	v_cmp_gt_i32_e64 s[28:29], 58, v182
	v_cndmask_b32_e64 v130, v130, v243, s[30:31]
	v_cmp_gt_i32_e64 s[30:31], 59, v182
	v_cmp_gt_i32_e64 s[26:27], 57, v182
	s_and_b64 s[28:29], s[30:31], s[28:29]
	v_cmp_gt_i32_e64 s[24:25], 56, v182
	s_and_b64 s[26:27], s[28:29], s[26:27]
	v_cmp_gt_i32_e64 s[22:23], 51, v182
	s_and_b64 s[24:25], s[26:27], s[24:25]
	v_cmp_gt_i32_e64 s[20:21], 50, v182
	s_and_b64 s[22:23], s[24:25], s[22:23]
	v_cmp_gt_i32_e64 s[18:19], 49, v182
	s_and_b64 s[20:21], s[22:23], s[20:21]
	v_cmp_gt_i32_e64 s[16:17], 48, v182
	s_and_b64 s[18:19], s[20:21], s[18:19]
	v_cmp_gt_i32_e64 s[14:15], 43, v182
	s_and_b64 s[16:17], s[18:19], s[16:17]
	v_cmp_gt_i32_e64 s[12:13], 42, v182
	s_and_b64 s[14:15], s[16:17], s[14:15]
	v_cmp_gt_i32_e64 s[10:11], 41, v182
	s_and_b64 s[12:13], s[14:15], s[12:13]
	v_cmp_gt_i32_e64 s[8:9], 40, v182
	s_and_b64 s[10:11], s[12:13], s[10:11]
	v_cmp_gt_i32_e64 s[6:7], 35, v182
	s_and_b64 s[8:9], s[10:11], s[8:9]
	v_cmp_gt_i32_e64 s[4:5], 34, v182
	s_and_b64 s[6:7], s[8:9], s[6:7]
	v_cmp_gt_i32_e64 s[2:3], 33, v182
	s_and_b64 s[4:5], s[6:7], s[4:5]
	v_cmp_gt_i32_e32 vcc, 32, v182
	s_and_b64 s[2:3], s[4:5], s[2:3]
	v_cndmask_b32_e64 v145, v145, v243, s[62:63]
	s_mov_b32 s62, 0x41200000
	v_cndmask_b32_e64 v144, v144, v243, s[60:61]
	s_mov_b32 s60, 2.0
	v_cndmask_b32_e64 v143, v143, v243, s[58:59]
	s_mov_b32 s58, 0x41800000
	s_and_b64 vcc, s[2:3], vcc
	s_mov_b32 s63, 0x41300000
	s_mov_b32 s61, 0x40400000
	s_mov_b32 s59, 0x41880000
	v_cndmask_b32_e64 v142, v142, v243, s[56:57]
	v_cndmask_b32_e64 v141, v141, v243, s[54:55]
	v_cndmask_b32_e64 v140, v140, v243, s[52:53]
	v_cndmask_b32_e64 v139, v139, v243, s[50:51]
	v_cndmask_b32_e64 v138, v138, v243, s[48:49]
	v_cndmask_b32_e64 v137, v137, v243, s[46:47]
	v_cndmask_b32_e64 v136, v136, v243, s[44:45]
	v_cndmask_b32_e64 v135, v135, v243, s[42:43]
	v_cndmask_b32_e64 v134, v134, v243, s[40:41]
	v_cndmask_b32_e64 v133, v133, v243, s[38:39]
	v_cndmask_b32_e64 v132, v132, v243, s[36:37]
	v_cndmask_b32_e64 v131, v131, v243, s[34:35]
	v_cndmask_b32_e64 v161, v161, v243, s[30:31]
	v_cndmask_b32_e64 v160, v160, v243, s[28:29]
	v_cndmask_b32_e64 v159, v159, v243, s[26:27]
	v_cndmask_b32_e64 v158, v158, v243, s[24:25]
	v_cndmask_b32_e64 v157, v157, v243, s[22:23]
	v_cndmask_b32_e64 v156, v156, v243, s[20:21]
	v_cndmask_b32_e64 v155, v155, v243, s[18:19]
	v_cndmask_b32_e64 v154, v154, v243, s[16:17]
	v_cndmask_b32_e64 v153, v153, v243, s[14:15]
	v_cndmask_b32_e64 v152, v152, v243, s[12:13]
	v_cndmask_b32_e64 v151, v151, v243, s[10:11]
	v_cndmask_b32_e64 v150, v150, v243, s[8:9]
	v_cndmask_b32_e64 v149, v149, v243, s[6:7]
	v_cndmask_b32_e64 v148, v148, v243, s[4:5]
	v_cndmask_b32_e64 v147, v147, v243, s[2:3]
	v_cndmask_b32_e32 v146, v146, v243, vcc

.Lmk_a1:
	s_mov_b32 s2, 0x41900000
	s_mov_b32 s3, 0x41980000
	v_fma_f32 v140, v196, s2, v146
	v_fma_f32 v141, v197, s3, v146
	s_mov_b32 s2, 0x41c00000
	s_mov_b32 s3, 0x41c80000
	v_fma_f32 v142, v196, s2, v146
	v_fma_f32 v143, v197, s3, v146
	s_mov_b32 s2, 0x41d00000
	s_mov_b32 s3, 0x41d80000
	v_fma_f32 v144, v196, s2, v146
	v_fma_f32 v145, v197, s3, v146
	s_mov_b32 s2, 0x42000000
	v_fma_f32 v131, -v190, v130, v190
	v_mov_b32_e32 v130, v146
	v_mov_b32_e32 v191, v190
	s_mov_b32 s3, 0x42040000
	v_fmac_f32_e32 v130, 0, v190
	v_fma_f32 v132, v196, s60, v146
	v_fma_f32 v133, v197, s61, v146
	v_fma_f32 v134, v196, s74, v146
	v_fma_f32 v135, v197, s75, v146
	v_fma_f32 v136, v196, s62, v146
	v_fma_f32 v137, v197, s63, v146
	v_fma_f32 v138, v196, s58, v146
	v_fma_f32 v139, v197, s59, v146
	v_fma_f32 v160, v190, s68, v146
	v_fma_f32 v161, v191, s69, v146
	v_fma_f32 v158, v190, s96, v146
	v_fma_f32 v159, v191, s97, v146
	v_fma_f32 v156, v190, s94, v146
	v_fma_f32 v157, v191, s95, v146
	v_fma_f32 v154, v190, s92, v146
	v_fma_f32 v155, v191, s93, v146
	v_fma_f32 v152, v190, s90, v146
	v_fma_f32 v153, v191, s91, v146
	v_fma_f32 v150, v190, s88, v146
	v_fma_f32 v151, v191, s89, v146
	v_fma_f32 v148, v190, s86, v146
	v_fma_f32 v149, v191, s87, v146
	v_fma_f32 v147, v193, s3, v146
	v_fma_f32 v146, v192, s2, v146
	s_setprio 1
	ds_read_b128 v[184:187], v218
	s_waitcnt lgkmcnt(0)
	v_mfma_f32_32x32x16_bf16 v[130:145], v[184:187], v[178:181], v[130:145]
	ds_read_b128 v[184:187], v218 offset:8192
	s_waitcnt lgkmcnt(0)
	v_mfma_f32_32x32x16_bf16 v[146:161], v[184:187], v[178:181], v[146:161]
	ds_read_b128 v[178:181], v217
	s_waitcnt lgkmcnt(0)
	v_mfma_f32_32x32x16_bf16 v[130:145], v[178:181], v[170:173], v[130:145]
	ds_read_b128 v[178:181], v217 offset:8192
	s_waitcnt lgkmcnt(0)
	v_mfma_f32_32x32x16_bf16 v[146:161], v[178:181], v[170:173], v[146:161]
	ds_read_b128 v[170:173], v216
	s_waitcnt lgkmcnt(0)
	v_mfma_f32_32x32x16_bf16 v[130:145], v[170:173], v[166:169], v[130:145]
	ds_read_b128 v[170:173], v216 offset:8192
	s_waitcnt lgkmcnt(0)
	v_mfma_f32_32x32x16_bf16 v[146:161], v[170:173], v[166:169], v[146:161]
	ds_read_b128 v[166:169], v215
	s_waitcnt lgkmcnt(0)
	v_mfma_f32_32x32x16_bf16 v[130:145], v[166:169], v[162:165], v[130:145]
	ds_read_b128 v[166:169], v215 offset:8192
	s_waitcnt lgkmcnt(0)
	v_mfma_f32_32x32x16_bf16 v[146:161], v[166:169], v[162:165], v[146:161]
	ds_read_b128 v[162:165], v218 offset:128
	s_waitcnt lgkmcnt(0)
	v_mfma_f32_32x32x16_bf16 v[130:145], v[162:165], v[174:177], v[130:145]
	ds_read_b128 v[162:165], v218 offset:8320
	s_waitcnt lgkmcnt(0)
	v_mfma_f32_32x32x16_bf16 v[146:161], v[162:165], v[174:177], v[146:161]
	ds_read_b128 v[162:165], v217 offset:128
	ds_read_b128 v[166:169], v205
	s_waitcnt lgkmcnt(0)
	v_mfma_f32_32x32x16_bf16 v[130:145], v[162:165], v[166:169], v[130:145]
	ds_read_b128 v[162:165], v217 offset:8320
	s_waitcnt lgkmcnt(0)
	v_mfma_f32_32x32x16_bf16 v[146:161], v[162:165], v[166:169], v[146:161]
	ds_read_b128 v[162:165], v216 offset:128
	ds_read_b128 v[166:169], v205 offset:1024
	s_waitcnt lgkmcnt(0)
	v_mfma_f32_32x32x16_bf16 v[130:145], v[162:165], v[166:169], v[130:145]
	ds_read_b128 v[162:165], v216 offset:8320
	s_waitcnt lgkmcnt(0)
	v_mfma_f32_32x32x16_bf16 v[146:161], v[162:165], v[166:169], v[146:161]
	ds_read_b128 v[162:165], v215 offset:128
	ds_read_b128 v[166:169], v205 offset:2048
	s_waitcnt lgkmcnt(0)
	v_mfma_f32_32x32x16_bf16 v[130:145], v[162:165], v[166:169], v[130:145]
	ds_read_b128 v[162:165], v215 offset:8320
	s_waitcnt lgkmcnt(0)
	v_mfma_f32_32x32x16_bf16 v[146:161], v[162:165], v[166:169], v[146:161]
	s_setprio 0
	s_add_i32 s72, s72, -1
	s_cmp_le_i32 s72, s65
	s_cbranch_scc1 .LBB0_1373
	v_cmp_gt_i32_e64 s[60:61], 26, v182
	v_cmp_gt_i32_e64 s[62:63], 27, v182
	v_cmp_gt_i32_e64 s[58:59], 25, v182
	s_and_b64 s[60:61], s[62:63], s[60:61]
	v_cmp_gt_i32_e64 s[56:57], 24, v182
	s_and_b64 s[58:59], s[60:61], s[58:59]
	v_cmp_gt_i32_e64 s[54:55], 19, v182
	s_and_b64 s[56:57], s[58:59], s[56:57]
	v_cmp_gt_i32_e64 s[52:53], 18, v182
	s_and_b64 s[54:55], s[56:57], s[54:55]
	v_cmp_gt_i32_e64 s[50:51], 17, v182
	s_and_b64 s[52:53], s[54:55], s[52:53]
	v_cmp_gt_i32_e64 s[48:49], 16, v182
	s_and_b64 s[50:51], s[52:53], s[50:51]
	v_cmp_gt_i32_e64 s[46:47], 11, v182
	s_and_b64 s[48:49], s[50:51], s[48:49]
	v_cmp_gt_i32_e64 s[44:45], 10, v182
	s_and_b64 s[46:47], s[48:49], s[46:47]
	v_cmp_gt_i32_e64 s[42:43], 9, v182
	s_and_b64 s[44:45], s[46:47], s[44:45]
	v_cmp_gt_i32_e64 s[40:41], 8, v182
	s_and_b64 s[42:43], s[44:45], s[42:43]
	v_cmp_gt_i32_e64 s[38:39], 3, v182
	s_and_b64 s[40:41], s[42:43], s[40:41]
	v_cmp_gt_i32_e64 s[36:37], 2, v182
	s_and_b64 s[38:39], s[40:41], s[38:39]
	v_cmp_gt_i32_e64 s[34:35], 1, v182
	s_and_b64 s[36:37], s[38:39], s[36:37]
	v_cmp_gt_i32_e64 s[30:31], 0, v182
	s_and_b64 s[34:35], s[36:37], s[34:35]
	s_and_b64 s[30:31], s[34:35], s[30:31]
	v_cmp_gt_i32_e64 s[28:29], 58, v182
	v_cndmask_b32_e64 v130, v130, v243, s[30:31]
	v_cmp_gt_i32_e64 s[30:31], 59, v182
	v_cmp_gt_i32_e64 s[26:27], 57, v182
	s_and_b64 s[28:29], s[30:31], s[28:29]
	v_cmp_gt_i32_e64 s[24:25], 56, v182
	s_and_b64 s[26:27], s[28:29], s[26:27]
	v_cmp_gt_i32_e64 s[22:23], 51, v182
	s_and_b64 s[24:25], s[26:27], s[24:25]
	v_cmp_gt_i32_e64 s[20:21], 50, v182
	s_and_b64 s[22:23], s[24:25], s[22:23]
	v_cmp_gt_i32_e64 s[18:19], 49, v182
	s_and_b64 s[20:21], s[22:23], s[20:21]
	v_cmp_gt_i32_e64 s[16:17], 48, v182
	s_and_b64 s[18:19], s[20:21], s[18:19]
	v_cmp_gt_i32_e64 s[14:15], 43, v182
	s_and_b64 s[16:17], s[18:19], s[16:17]
	v_cmp_gt_i32_e64 s[12:13], 42, v182
	s_and_b64 s[14:15], s[16:17], s[14:15]
	v_cmp_gt_i32_e64 s[10:11], 41, v182
	s_and_b64 s[12:13], s[14:15], s[12:13]
	v_cmp_gt_i32_e64 s[8:9], 40, v182
	s_and_b64 s[10:11], s[12:13], s[10:11]
	v_cmp_gt_i32_e64 s[6:7], 35, v182
	s_and_b64 s[8:9], s[10:11], s[8:9]
	v_cmp_gt_i32_e64 s[4:5], 34, v182
	s_and_b64 s[6:7], s[8:9], s[6:7]
	v_cmp_gt_i32_e64 s[2:3], 33, v182
	s_and_b64 s[4:5], s[6:7], s[4:5]
	v_cmp_gt_i32_e32 vcc, 32, v182
	s_and_b64 s[2:3], s[4:5], s[2:3]
	v_cndmask_b32_e64 v145, v145, v243, s[62:63]
	s_mov_b32 s62, 0x41200000
	v_cndmask_b32_e64 v144, v144, v243, s[60:61]
	s_mov_b32 s60, 2.0
	v_cndmask_b32_e64 v143, v143, v243, s[58:59]
	s_mov_b32 s58, 0x41800000
	s_and_b64 vcc, s[2:3], vcc
	s_mov_b32 s63, 0x41300000
	s_mov_b32 s61, 0x40400000
	s_mov_b32 s59, 0x41880000
	v_cndmask_b32_e64 v142, v142, v243, s[56:57]
	v_cndmask_b32_e64 v141, v141, v243, s[54:55]
	v_cndmask_b32_e64 v140, v140, v243, s[52:53]
	v_cndmask_b32_e64 v139, v139, v243, s[50:51]
	v_cndmask_b32_e64 v138, v138, v243, s[48:49]
	v_cndmask_b32_e64 v137, v137, v243, s[46:47]
	v_cndmask_b32_e64 v136, v136, v243, s[44:45]
	v_cndmask_b32_e64 v135, v135, v243, s[42:43]
	v_cndmask_b32_e64 v134, v134, v243, s[40:41]
	v_cndmask_b32_e64 v133, v133, v243, s[38:39]
	v_cndmask_b32_e64 v132, v132, v243, s[36:37]
	v_cndmask_b32_e64 v131, v131, v243, s[34:35]
	v_cndmask_b32_e64 v161, v161, v243, s[30:31]
	v_cndmask_b32_e64 v160, v160, v243, s[28:29]
	v_cndmask_b32_e64 v159, v159, v243, s[26:27]
	v_cndmask_b32_e64 v158, v158, v243, s[24:25]
	v_cndmask_b32_e64 v157, v157, v243, s[22:23]
	v_cndmask_b32_e64 v156, v156, v243, s[20:21]
	v_cndmask_b32_e64 v155, v155, v243, s[18:19]
	v_cndmask_b32_e64 v154, v154, v243, s[16:17]
	v_cndmask_b32_e64 v153, v153, v243, s[14:15]
	v_cndmask_b32_e64 v152, v152, v243, s[12:13]
	v_cndmask_b32_e64 v151, v151, v243, s[10:11]
	v_cndmask_b32_e64 v150, v150, v243, s[8:9]
	v_cndmask_b32_e64 v149, v149, v243, s[6:7]
	v_cndmask_b32_e64 v148, v148, v243, s[4:5]
	v_cndmask_b32_e64 v147, v147, v243, s[2:3]
	v_cndmask_b32_e32 v146, v146, v243, vcc
